# combined version plus pool window-loop LDS read-ahead and attention V^T pitch 264
# baseline (speedup 1.0000x reference)
; #define LAS __attribute__((address_space(3)))
; __device__ __forceinline__ void cvt8(const u32x4 r, float (&f)[8]) { f[0] = bflo(r.x); f[1] = bfhi(r.x); f[2] = bflo(r.y); f[3] = bfhi(r.y); f[4] = bflo(r.z); f[5] = bfhi(r.z); f[6] = bflo(r.w); f[7] = bfhi(r.w); }
; __device__ __forceinline__ bf16x8 pack8(const float (&f)[8]) { u32x4 w; w.x = pk2(f[0], f[1]); w.y = pk2(f[2], f[3]); w.z = pk2(f[4], f[5]); w.w = pk2(f[6], f[7]); return __builtin_bit_cast(bf16x8, w); }
; __device__ __forceinline__ void pool_unit(Ctx& C, int l, int blk) {
;     ...
;         for (int k = 0; k < 4; ++k) { const int tt = 4 * tg + k, t = t0 + tt; const int lo = max(t - hw, 0), hi = min(t + hw, L);
;             float sacc[8];
; #pragma unroll
;             for (int j = 0; j < 8; ++j) sacc[j] = 0.f;
;             for (int q = lo; q < hi; ++q) { float f[8]; cvt8(*(const LAS u32x4*)(C.lds + (q - t0 + 8) * RS + c8 * 16), f);
; #pragma unroll
;                 for (int j = 0; j < 8; ++j) sacc[j] += f[j]; }
;             float cf[8]; cvt8(*(const LAS u32x4*)(C.lds + (tt + 8) * RS + c8 * 16), cf); const float inv = 1.0f / (float)(hi - lo);
; #pragma unroll
;             for (int j = 0; j < 8; ++j) sacc[j] = sacc[j] * inv - cf[j];
;             *(LAS bf16x8*)(C.lds + DT_OFF + tt * RS + c8 * 16) = pack8(sacc); }
.LBB0_480:
	v_or_b32_e32 v18, s14, v16
	v_add_u32_e32 v6, s13, v18
	v_sub_u32_e32 v7, v6, v5
	v_add_u32_e32 v6, v6, v5
	v_max_i32_e32 v19, 0, v7
	v_min_i32_e32 v20, s11, v6
	v_mov_b32_e32 v9, 0
	v_cmp_gt_i32_e32 vcc, v20, v19
	v_mov_b32_e32 v8, v9
	v_mov_b32_e32 v11, v9
	v_mov_b32_e32 v10, v9
	v_mov_b32_e32 v13, v9
	v_mov_b32_e32 v12, v9
	v_mov_b32_e32 v7, v9
	v_mov_b32_e32 v6, v9
	s_and_saveexec_b64 s[6:7], vcc
	s_cbranch_execz .LBB0_479
	v_max_i32_e32 v6, 0, v17
	v_add_u32_e32 v6, s12, v6
	v_mad_u64_u32 v[14:15], s[8:9], v6, s71, v[4:5]
	v_mov_b32_e32 v6, 0
	s_mov_b64 s[8:9], 0
	v_mov_b32_e32 v15, v19
	v_mov_b32_e32 v7, v6
	v_mov_b32_e32 v12, v6
	v_mov_b32_e32 v13, v6
	v_mov_b32_e32 v10, v6
	v_mov_b32_e32 v11, v6
	v_mov_b32_e32 v8, v6
	v_mov_b32_e32 v9, v6
	ds_read_b128 v[244:247], v14
	v_add_u32_e32 v14, 0x410, v14
.LBB0_482:
	s_waitcnt lgkmcnt(0)
	v_mov_b32_e32 v22, v244
	v_mov_b32_e32 v23, v245
	v_mov_b32_e32 v24, v246
	v_mov_b32_e32 v25, v247
	ds_read_b128 v[244:247], v14
	v_add_u32_e32 v15, 1, v15
	v_cmp_ge_i32_e32 vcc, v15, v20
	v_add_u32_e32 v14, 0x410, v14
	s_or_b64 s[8:9], vcc, s[8:9]
	v_lshlrev_b32_e32 v26, 16, v22
	v_and_b32_e32 v27, 0xffff0000, v22
	v_lshlrev_b32_e32 v22, 16, v23
	v_and_b32_e32 v23, 0xffff0000, v23
	v_lshlrev_b32_e32 v28, 16, v24
	v_and_b32_e32 v29, 0xffff0000, v24
	v_lshlrev_b32_e32 v24, 16, v25
	v_and_b32_e32 v25, 0xffff0000, v25
	v_pk_add_f32 v[12:13], v[12:13], v[26:27]
	v_pk_add_f32 v[10:11], v[10:11], v[22:23]
	v_pk_add_f32 v[8:9], v[8:9], v[28:29]
	v_pk_add_f32 v[6:7], v[6:7], v[24:25]
	s_andn2_b64 exec, exec, s[8:9]
	s_cbranch_execnz .LBB0_482
	s_or_b64 exec, exec, s[8:9]
	s_branch .LBB0_479

; __device__ __forceinline__ void cvt8(const u32x4 r, float (&f)[8]) { f[0] = bflo(r.x); f[1] = bfhi(r.x); f[2] = bflo(r.y); f[3] = bfhi(r.y); f[4] = bflo(r.z); f[5] = bfhi(r.z); f[6] = bflo(r.w); f[7] = bfhi(r.w); }
; __device__ __forceinline__ bf16x8 pack8(const float (&f)[8]) { u32x4 w; w.x = pk2(f[0], f[1]); w.y = pk2(f[2], f[3]); w.z = pk2(f[4], f[5]); w.w = pk2(f[6], f[7]); return __builtin_bit_cast(bf16x8, w); }
; __device__ __forceinline__ void attn_unit(Ctx& C, int l, int uidx) {
;     ...
;     if (!isctx) { b = uidx >> 6; kh = (uidx >> 5) & 1; nb = uidx & 31; } else { const int v = uidx - 256; b = v >> 2; kh = (v >> 1) & 1; nb = v & 1; }
;     const int rowbase = isctx ? NLAT + b * CL : b * SL, crow = NLAT + b * CL;
;     const int g = C.wave >> 1, th = C.wave & 1, head = kh * 4 + g, r32 = C.lane & 31, h = C.lane >> 5;
;     const bf16* Z = WSP(bf16, WS_Z); const f32x2* ROPE = WSP(f32x2, WS_ROPE);
;     bf16x8 Qf[2][4];
; #pragma unroll
;     for (int qb = 0; qb < 2; ++qb) {
;         const int tq = 128 * nb + 64 * th + 32 * qb + r32;
;         const bf16* qp = Z + (size_t)(rowbase + tq) * INW + 512 + 64 * head + 8 * h;
;         float f[4][8];
; #pragma unroll
;         for (int s = 0; s < 4; ++s) cvt8(*(const u32x4*)(qp + 16 * s), f[s]);
;         if (!isctx) {
;             const int pr = tq >> 6, pc = tq & 63;
; #pragma unroll
;             for (int j = 0; j < 8; ++j) {
;                 const f32x2 cr = ROPE[pr * 16 + 8 * h + j], cc = ROPE[pc * 16 + 8 * h + j];
;                 const float a0 = f[0][j], b0 = f[1][j]; f[0][j] = a0 * cr.x - b0 * cr.y; f[1][j] = b0 * cr.x + a0 * cr.y;
;                 const float a1 = f[2][j], b1 = f[3][j]; f[2][j] = a1 * cc.x - b1 * cc.y; f[3][j] = b1 * cc.x + a1 * cc.y; }
;         }
; #pragma unroll
;         for (int s = 0; s < 4; ++s) {
; #pragma unroll
;             for (int j = 0; j < 8; ++j) f[s][j] *= 0.125f * LOG2E;
;             Qf[qb][s] = pack8(f[s]); }
;     }
.LBB0_576:
	s_andn2_b64 vcc, exec, s[6:7]
	s_cbranch_vccnz .LBB0_792
	s_ashr_i32 s6, s43, 6
	s_bfe_u32 s18, s43, 0x10005
	s_and_b32 s8, s43, 31
	s_lshl_b32 s19, s6, 8
	s_lshl_b32 s43, s6, 12
	s_ashr_i32 s6, s51, 7
	s_lshl_b32 s7, s18, 2
	s_bfe_u32 s9, s51, 0x10006
	s_add_i32 s6, s6, s7
	s_add_u32 s10, s54, 0x36000000
	s_addc_u32 s11, s55, 0
	s_add_u32 s14, s54, 0x200000
	s_addc_u32 s15, s55, 0
	s_lshl_b32 s7, s8, 7
	s_lshl_b32 s58, s9, 6
	v_and_b32_e32 v48, 31, v178
	v_lshrrev_b32_e32 v50, 5, v162
	s_or_b32 s7, s58, s7
	v_or_b32_e32 v51, s7, v48
	s_lshl_b32 s12, s6, 6
	v_lshlrev_b32_e32 v49, 3, v50
	s_lshr_b32 s7, s7, 2
	v_or_b32_e32 v2, s7, v49
	s_ashr_i32 s13, s12, 31
	v_or_b32_e32 v160, s43, v51
	v_mov_b64_e32 v[44:45], s[10:11]
	v_lshlrev_b32_e32 v2, 3, v2
	v_mad_i64_i32 v[20:21], s[26:27], v160, s66, v[44:45]
	s_lshl_b64 s[12:13], s[12:13], 1
	global_load_dwordx4 v[12:15], v2, s[14:15] offset:16
	global_load_dwordx4 v[16:19], v2, s[14:15]
	global_load_dwordx4 v[4:7], v2, s[14:15] offset:48
	global_load_dwordx4 v[8:11], v2, s[14:15] offset:32
	v_lshl_add_u64 v[20:21], v[20:21], 0, s[12:13]
	v_lshlrev_b32_e32 v2, 4, v50
	v_lshl_add_u64 v[20:21], v[20:21], 0, v[2:3]
	global_load_dwordx4 v[52:55], v[20:21], off offset:1024
	global_load_dwordx4 v[56:59], v[20:21], off offset:1056
	global_load_dwordx4 v[24:27], v[20:21], off offset:1088
	global_load_dwordx4 v[28:31], v[20:21], off offset:1120
	v_lshlrev_b32_e32 v22, 6, v50
	v_lshl_or_b32 v32, v48, 7, v22
	global_load_dwordx4 v[40:43], v32, s[14:15]
	global_load_dwordx4 v[36:39], v32, s[14:15] offset:16
	global_load_dwordx4 v[20:23], v32, s[14:15] offset:48
	s_nop 0
	global_load_dwordx4 v[32:35], v32, s[14:15] offset:32
	v_or_b32_e32 v51, 32, v51
	s_movk_i32 s7, 0x3f0
	v_ashrrev_i32_e32 v159, 3, v178
	v_lshlrev_b32_e32 v180, 2, v50
	v_ashrrev_i32_e32 v161, 31, v160
	v_and_b32_e32 v181, 63, v159
	v_mov_b32_e32 v191, 1.0
	v_mov_b32_e32 v193, 1.0
	s_waitcnt vmcnt(0)
	v_mov_b32_e32 v46, v16
	v_mov_b32_e32 v47, v18
	v_mov_b32_e32 v18, v17
	v_mov_b32_e32 v16, v12
	v_mov_b32_e32 v17, v14
	v_mov_b32_e32 v14, v13
	v_lshlrev_b32_e32 v60, 16, v56
	v_and_b32_e32 v61, 0xffff0000, v56
	v_lshlrev_b32_e32 v56, 16, v57
	v_and_b32_e32 v57, 0xffff0000, v57
	v_mov_b32_e32 v12, v8
	v_mov_b32_e32 v13, v10
	v_mov_b32_e32 v10, v9
	v_mov_b32_e32 v8, v4
	v_mov_b32_e32 v9, v6
	v_mov_b32_e32 v6, v5
	v_lshlrev_b32_e32 v4, 16, v52
	v_and_b32_e32 v5, 0xffff0000, v52
	v_lshlrev_b32_e32 v52, 16, v53
	v_and_b32_e32 v53, 0xffff0000, v53
	v_lshlrev_b32_e32 v62, 16, v54
	v_and_b32_e32 v63, 0xffff0000, v54
	v_lshlrev_b32_e32 v64, 16, v58
	v_and_b32_e32 v65, 0xffff0000, v58
	v_lshlrev_b32_e32 v66, 16, v55
	v_and_b32_e32 v67, 0xffff0000, v55
	v_lshlrev_b32_e32 v54, 16, v59
	v_and_b32_e32 v55, 0xffff0000, v59
	v_pk_mul_f32 v[58:59], v[46:47], v[60:61]
	v_pk_mul_f32 v[60:61], v[18:19], v[60:61]
	v_pk_mul_f32 v[68:69], v[16:17], v[56:57]
	v_pk_mul_f32 v[56:57], v[14:15], v[56:57]
	v_pk_fma_f32 v[58:59], v[18:19], v[4:5], v[58:59]
	v_pk_fma_f32 v[4:5], v[46:47], v[4:5], v[60:61] neg_lo:[0,0,1] neg_hi:[0,0,1]
	v_pk_fma_f32 v[60:61], v[14:15], v[52:53], v[68:69]
	v_pk_fma_f32 v[52:53], v[16:17], v[52:53], v[56:57] neg_lo:[0,0,1] neg_hi:[0,0,1]
	v_pk_mul_f32 v[70:71], v[12:13], v[64:65]
	v_pk_mul_f32 v[52:53], v[52:53], s[42:43] op_sel_hi:[1,0]
	v_pk_mul_f32 v[64:65], v[10:11], v[64:65]
	v_cvt_pk_bf16_f32 v99, v52, v53
	v_or_b32_e32 v52, s43, v51
	v_mad_i64_i32 v[52:53], s[26:27], v52, s66, v[44:45]
	v_pk_fma_f32 v[56:57], v[10:11], v[62:63], v[70:71]
	v_pk_fma_f32 v[62:63], v[12:13], v[62:63], v[64:65] neg_lo:[0,0,1] neg_hi:[0,0,1]
	v_lshl_add_u64 v[52:53], v[52:53], 0, s[12:13]
	v_pk_mul_f32 v[72:73], v[8:9], v[54:55]
	v_pk_mul_f32 v[4:5], v[4:5], s[42:43] op_sel_hi:[1,0]
	v_pk_mul_f32 v[64:65], v[58:59], s[42:43] op_sel_hi:[1,0]
	v_pk_mul_f32 v[58:59], v[62:63], s[42:43] op_sel_hi:[1,0]
	v_pk_mul_f32 v[62:63], v[56:57], s[42:43] op_sel_hi:[1,0]
	v_pk_mul_f32 v[56:57], v[6:7], v[54:55]
	v_lshl_add_u64 v[68:69], v[52:53], 0, v[2:3]
	v_cvt_pk_bf16_f32 v98, v4, v5
	v_cvt_pk_bf16_f32 v100, v58, v59
	v_pk_fma_f32 v[4:5], v[6:7], v[66:67], v[72:73]
	global_load_dwordx4 v[52:55], v[68:69], off offset:1024
	v_pk_fma_f32 v[66:67], v[8:9], v[66:67], v[56:57] neg_lo:[0,0,1] neg_hi:[0,0,1]
	global_load_dwordx4 v[56:59], v[68:69], off offset:1056
	v_pk_mul_f32 v[60:61], v[60:61], s[42:43] op_sel_hi:[1,0]
	v_pk_mul_f32 v[4:5], v[4:5], s[42:43] op_sel_hi:[1,0]
	v_cvt_pk_bf16_f32 v103, v60, v61
	v_cvt_pk_bf16_f32 v104, v62, v63
	v_lshlrev_b32_e32 v60, 16, v28
	v_and_b32_e32 v61, 0xffff0000, v28
	v_mov_b32_e32 v62, v40
	v_mov_b32_e32 v63, v42
	v_cvt_pk_bf16_f32 v102, v64, v65
	v_cvt_pk_bf16_f32 v105, v4, v5
	v_lshlrev_b32_e32 v4, 16, v24
	v_and_b32_e32 v5, 0xffff0000, v24
	v_pk_mul_f32 v[64:65], v[62:63], v[60:61]
	v_mov_b32_e32 v42, v41
	v_pk_fma_f32 v[40:41], v[42:43], v[4:5], v[64:65]
	v_pk_mul_f32 v[42:43], v[42:43], v[60:61]
	v_lshlrev_b32_e32 v28, 16, v29
	v_pk_fma_f32 v[4:5], v[62:63], v[4:5], v[42:43] neg_lo:[0,0,1] neg_hi:[0,0,1]
	v_and_b32_e32 v29, 0xffff0000, v29
	v_pk_mul_f32 v[4:5], v[4:5], s[42:43] op_sel_hi:[1,0]
	v_lshlrev_b32_e32 v24, 16, v25
	v_cvt_pk_bf16_f32 v106, v4, v5
	v_pk_mul_f32 v[4:5], v[40:41], s[42:43] op_sel_hi:[1,0]
	v_mov_b32_e32 v40, v36
	v_mov_b32_e32 v41, v38
	v_mov_b32_e32 v38, v37
	v_and_b32_e32 v25, 0xffff0000, v25
	v_pk_mul_f32 v[42:43], v[40:41], v[28:29]
	v_pk_mul_f32 v[28:29], v[38:39], v[28:29]
	v_pk_fma_f32 v[36:37], v[38:39], v[24:25], v[42:43]
	v_pk_fma_f32 v[24:25], v[40:41], v[24:25], v[28:29] neg_lo:[0,0,1] neg_hi:[0,0,1]
	v_pk_mul_f32 v[66:67], v[66:67], s[42:43] op_sel_hi:[1,0]
; __device__ __forceinline__ void cvt8(const u32x4 r, float (&f)[8]) { f[0] = bflo(r.x); f[1] = bfhi(r.x); f[2] = bflo(r.y); f[3] = bfhi(r.y); f[4] = bflo(r.z); f[5] = bfhi(r.z); f[6] = bflo(r.w); f[7] = bfhi(r.w); }
; __device__ __forceinline__ bf16x8 pack8(const float (&f)[8]) { u32x4 w; w.x = pk2(f[0], f[1]); w.y = pk2(f[2], f[3]); w.z = pk2(f[4], f[5]); w.w = pk2(f[6], f[7]); return __builtin_bit_cast(bf16x8, w); }
; __device__ __forceinline__ void attn_unit(Ctx& C, int l, int uidx) {
;     ...
;     for (int qb = 0; qb < 2; ++qb) {
;         const int tq = 128 * nb + 64 * th + 32 * qb + r32;
;         const bf16* qp = Z + (size_t)(rowbase + tq) * INW + 512 + 64 * head + 8 * h;
;         float f[4][8];
; #pragma unroll
;         for (int s = 0; s < 4; ++s) cvt8(*(const u32x4*)(qp + 16 * s), f[s]);
;         if (!isctx) {
;             const int pr = tq >> 6, pc = tq & 63;
; #pragma unroll
;             for (int j = 0; j < 8; ++j) {
;                 const f32x2 cr = ROPE[pr * 16 + 8 * h + j], cc = ROPE[pc * 16 + 8 * h + j];
;                 const float a0 = f[0][j], b0 = f[1][j]; f[0][j] = a0 * cr.x - b0 * cr.y; f[1][j] = b0 * cr.x + a0 * cr.y;
;                 const float a1 = f[2][j], b1 = f[3][j]; f[2][j] = a1 * cc.x - b1 * cc.y; f[3][j] = b1 * cc.x + a1 * cc.y; }
;         }
; #pragma unroll
;         for (int s = 0; s < 4; ++s) {
; #pragma unroll
;             for (int j = 0; j < 8; ++j) f[s][j] *= 0.125f * LOG2E;
;             Qf[qb][s] = pack8(f[s]); }
;     }
;     float m_[2], l_[2]; f32x16 O[2][2];
;     { const float sk = INP(I_SINK)[l * 8 + head] * LOG2E; m_[0] = sk; m_[1] = sk; l_[0] = 1.f; l_[1] = 1.f; }
; #pragma unroll
;     for (int a = 0; a < 2; ++a)
; #pragma unroll
;         for (int q = 0; q < 2; ++q)
; #pragma unroll
;             for (int i = 0; i < 16; ++i) O[a][q][i] = 0.f;
;     ...
;     __syncthreads();
;     u32x4 kraw[2], kpar[2], vraw[2];
;     kpar[0] = (u32x4){0u, 0u, 0u, 0u}; kpar[1] = kpar[0];
;     int tt = isctx ? 3 : (nb == 0 ? 1 : 0);
;     AT_PREFETCH(tt);
	v_pk_mul_f32 v[24:25], v[24:25], s[42:43] op_sel_hi:[1,0]
	v_cvt_pk_bf16_f32 v101, v66, v67
	v_cvt_pk_bf16_f32 v107, v24, v25
	v_lshlrev_b32_e32 v24, 16, v26
	v_and_b32_e32 v25, 0xffff0000, v26
	v_lshlrev_b32_e32 v26, 4, v51
	v_lshlrev_b32_e32 v28, 16, v30
	v_and_b32_e32 v29, 0xffff0000, v30
	v_mov_b32_e32 v66, v32
	v_mov_b32_e32 v67, v34
	v_and_or_b32 v26, v26, s7, v49
	v_pk_mul_f32 v[64:65], v[36:37], s[42:43] op_sel_hi:[1,0]
	v_pk_mul_f32 v[36:37], v[66:67], v[28:29]
	v_mov_b32_e32 v34, v33
	v_lshlrev_b32_e32 v51, 3, v26
	v_pk_fma_f32 v[32:33], v[34:35], v[24:25], v[36:37]
	global_load_dwordx4 v[40:43], v[68:69], off offset:1088
	global_load_dwordx4 v[36:39], v[68:69], off offset:1120
	s_nop 0
	global_load_dwordx2 v[68:69], v51, s[14:15]
	global_load_dwordx4 v[60:63], v51, s[14:15] offset:8
	v_pk_mul_f32 v[28:29], v[34:35], v[28:29]
	v_lshlrev_b32_e32 v34, 16, v27
	v_pk_fma_f32 v[24:25], v[66:67], v[24:25], v[28:29] neg_lo:[0,0,1] neg_hi:[0,0,1]
	v_and_b32_e32 v35, 0xffff0000, v27
	v_pk_mul_f32 v[24:25], v[24:25], s[42:43] op_sel_hi:[1,0]
	v_lshlrev_b32_e32 v66, 16, v31
	v_cvt_pk_bf16_f32 v108, v24, v25
	v_and_b32_e32 v67, 0xffff0000, v31
	global_load_dwordx4 v[24:27], v51, s[14:15] offset:40
	global_load_dwordx4 v[28:31], v51, s[14:15] offset:24
	v_mov_b32_e32 v70, v20
	v_mov_b32_e32 v71, v22
	v_pk_mul_f32 v[72:73], v[70:71], v[66:67]
	v_mov_b32_e32 v22, v21
	v_pk_fma_f32 v[20:21], v[22:23], v[34:35], v[72:73]
	v_pk_mul_f32 v[22:23], v[22:23], v[66:67]
	v_pk_mul_f32 v[32:33], v[32:33], s[42:43] op_sel_hi:[1,0]
	v_pk_fma_f32 v[22:23], v[70:71], v[34:35], v[22:23] neg_lo:[0,0,1] neg_hi:[0,0,1]
	v_pk_mul_f32 v[20:21], v[20:21], s[42:43] op_sel_hi:[1,0]
	v_pk_mul_f32 v[22:23], v[22:23], s[42:43] op_sel_hi:[1,0]
	v_cvt_pk_bf16_f32 v112, v32, v33
	v_cvt_pk_bf16_f32 v109, v22, v23
	v_cvt_pk_bf16_f32 v113, v20, v21
	s_load_dwordx2 s[26:27], s[56:57], 0x58
	v_cvt_pk_bf16_f32 v110, v4, v5
	global_load_dwordx2 v[4:5], v51, s[14:15] offset:56
	s_ashr_i32 s7, s6, 31
	s_lshl_b64 s[6:7], s[6:7], 2
	s_waitcnt vmcnt(0)
	v_lshlrev_b32_e32 v20, 16, v52
	v_and_b32_e32 v21, 0xffff0000, v52
	v_lshlrev_b32_e32 v22, 16, v56
	v_and_b32_e32 v23, 0xffff0000, v56
	v_pk_mul_f32 v[32:33], v[46:47], v[22:23]
	s_waitcnt lgkmcnt(0)
	s_add_u32 s6, s26, s6
	v_pk_fma_f32 v[32:33], v[18:19], v[20:21], v[32:33]
	v_pk_mul_f32 v[18:19], v[18:19], v[22:23]
	v_lshlrev_b32_e32 v22, 16, v57
	v_pk_fma_f32 v[18:19], v[46:47], v[20:21], v[18:19] neg_lo:[0,0,1] neg_hi:[0,0,1]
	v_and_b32_e32 v23, 0xffff0000, v57
	v_pk_mul_f32 v[18:19], v[18:19], s[42:43] op_sel_hi:[1,0]
	v_lshlrev_b32_e32 v20, 16, v53
	v_cvt_pk_bf16_f32 v114, v18, v19
	v_pk_mul_f32 v[18:19], v[32:33], s[42:43] op_sel_hi:[1,0]
	v_and_b32_e32 v21, 0xffff0000, v53
	v_pk_mul_f32 v[32:33], v[16:17], v[22:23]
	s_addc_u32 s7, s27, s7
	v_pk_fma_f32 v[32:33], v[14:15], v[20:21], v[32:33]
	v_pk_mul_f32 v[14:15], v[14:15], v[22:23]
	s_lshl_b32 s38, s18, 7
	v_pk_fma_f32 v[14:15], v[16:17], v[20:21], v[14:15] neg_lo:[0,0,1] neg_hi:[0,0,1]
	v_lshlrev_b32_e32 v20, 16, v58
	v_and_b32_e32 v21, 0xffff0000, v58
	v_lshlrev_b32_e32 v16, 16, v54
	v_and_b32_e32 v17, 0xffff0000, v54
	v_pk_mul_f32 v[22:23], v[12:13], v[20:21]
	v_pk_mul_f32 v[14:15], v[14:15], s[42:43] op_sel_hi:[1,0]
	v_pk_fma_f32 v[22:23], v[10:11], v[16:17], v[22:23]
	v_pk_mul_f32 v[10:11], v[10:11], v[20:21]
	v_cvt_pk_bf16_f32 v115, v14, v15
	v_pk_fma_f32 v[10:11], v[12:13], v[16:17], v[10:11] neg_lo:[0,0,1] neg_hi:[0,0,1]
	v_lshlrev_b32_e32 v16, 16, v59
	v_and_b32_e32 v17, 0xffff0000, v59
	v_lshlrev_b32_e32 v12, 16, v55
	v_and_b32_e32 v13, 0xffff0000, v55
	v_pk_mul_f32 v[20:21], v[8:9], v[16:17]
	v_pk_mul_f32 v[10:11], v[10:11], s[42:43] op_sel_hi:[1,0]
	v_pk_fma_f32 v[20:21], v[6:7], v[12:13], v[20:21]
	v_pk_mul_f32 v[6:7], v[6:7], v[16:17]
	v_cvt_pk_bf16_f32 v116, v10, v11
	v_pk_fma_f32 v[6:7], v[8:9], v[12:13], v[6:7] neg_lo:[0,0,1] neg_hi:[0,0,1]
	v_pk_mul_f32 v[10:11], v[22:23], s[42:43] op_sel_hi:[1,0]
	v_pk_mul_f32 v[6:7], v[6:7], s[42:43] op_sel_hi:[1,0]
	v_cvt_pk_bf16_f32 v120, v10, v11
	v_cvt_pk_bf16_f32 v117, v6, v7
	v_pk_mul_f32 v[6:7], v[20:21], s[42:43] op_sel_hi:[1,0]
	v_pk_mul_f32 v[14:15], v[32:33], s[42:43] op_sel_hi:[1,0]
	v_cvt_pk_bf16_f32 v121, v6, v7
	v_cvt_pk_bf16_f32 v119, v14, v15
	v_lshlrev_b32_e32 v6, 16, v40
	v_lshlrev_b32_e32 v8, 16, v36
	v_and_b32_e32 v9, 0xffff0000, v36
	v_mov_b32_e32 v10, v68
	v_mov_b32_e32 v11, v60
	v_mov_b32_e32 v60, v69
	v_and_b32_e32 v7, 0xffff0000, v40
	v_pk_mul_f32 v[12:13], v[10:11], v[8:9]
	v_pk_mul_f32 v[8:9], v[60:61], v[8:9]
	v_pk_fma_f32 v[12:13], v[60:61], v[6:7], v[12:13]
	v_pk_fma_f32 v[6:7], v[10:11], v[6:7], v[8:9] neg_lo:[0,0,1] neg_hi:[0,0,1]
	v_lshlrev_b32_e32 v10, 16, v37
	v_pk_mul_f32 v[6:7], v[6:7], s[42:43] op_sel_hi:[1,0]
	v_and_b32_e32 v11, 0xffff0000, v37
	v_cvt_pk_bf16_f32 v122, v6, v7
	v_pk_mul_f32 v[6:7], v[12:13], s[42:43] op_sel_hi:[1,0]
	v_mov_b32_e32 v12, v62
	v_mov_b32_e32 v13, v28
	v_mov_b32_e32 v28, v63
	v_lshlrev_b32_e32 v8, 16, v41
	v_and_b32_e32 v9, 0xffff0000, v41
	v_pk_mul_f32 v[14:15], v[12:13], v[10:11]
	v_pk_mul_f32 v[10:11], v[28:29], v[10:11]
	v_pk_fma_f32 v[14:15], v[28:29], v[8:9], v[14:15]
	v_pk_fma_f32 v[8:9], v[12:13], v[8:9], v[10:11] neg_lo:[0,0,1] neg_hi:[0,0,1]
	v_lshlrev_b32_e32 v12, 16, v38
	v_pk_mul_f32 v[8:9], v[8:9], s[42:43] op_sel_hi:[1,0]
	v_and_b32_e32 v13, 0xffff0000, v38
	v_cvt_pk_bf16_f32 v123, v8, v9
	v_pk_mul_f32 v[8:9], v[14:15], s[42:43] op_sel_hi:[1,0]
	v_mov_b32_e32 v14, v30
	v_mov_b32_e32 v15, v24
	v_mov_b32_e32 v24, v31
	v_lshlrev_b32_e32 v10, 16, v42
	v_and_b32_e32 v11, 0xffff0000, v42
	v_pk_mul_f32 v[16:17], v[14:15], v[12:13]
	v_pk_mul_f32 v[12:13], v[24:25], v[12:13]
	v_sub_co_u32_e64 v23, vcc, s8, 1
	v_pk_fma_f32 v[16:17], v[24:25], v[10:11], v[16:17]
	v_pk_fma_f32 v[10:11], v[14:15], v[10:11], v[12:13] neg_lo:[0,0,1] neg_hi:[0,0,1]
	v_cndmask_b32_e64 v24, 0, 1, vcc
	v_addc_co_u32_e32 v14, vcc, 0, v23, vcc
	v_lshlrev_b32_e32 v14, 7, v14
	v_add_u32_e32 v25, s43, v14
	v_lshlrev_b32_e32 v28, 3, v178
	v_add_u32_e32 v14, v159, v25
	global_load_dword v22, v3, s[6:7]
	v_pk_mul_f32 v[10:11], v[10:11], s[42:43] op_sel_hi:[1,0]
	v_and_b32_e32 v162, 56, v28
	v_mad_i64_i32 v[14:15], s[6:7], v14, s66, v[44:45]
	v_cvt_pk_bf16_f32 v124, v10, v11
	v_pk_mul_f32 v[10:11], v[16:17], s[42:43] op_sel_hi:[1,0]
	v_lshl_add_u64 v[14:15], v[14:15], 0, s[38:39]
	v_lshlrev_b32_e32 v16, 1, v162
	v_mov_b32_e32 v17, v3
	v_cvt_pk_bf16_f32 v118, v18, v19
	v_lshl_add_u64 v[18:19], v[14:15], 0, v[16:17]
	s_barrier
; #define LAS __attribute__((address_space(3)))
; __device__ __forceinline__ void attn_unit(Ctx& C, int l, int uidx) {
;     ...
;     float m_[2], l_[2]; f32x16 O[2][2];
;     { const float sk = INP(I_SINK)[l * 8 + head] * LOG2E; m_[0] = sk; m_[1] = sk; l_[0] = 1.f; l_[1] = 1.f; }
; #pragma unroll
;     for (int a = 0; a < 2; ++a)
; #pragma unroll
;         for (int q = 0; q < 2; ++q)
; #pragma unroll
;             for (int i = 0; i < 16; ++i) O[a][q][i] = 0.f;
;     ...
;     __syncthreads();
;     u32x4 kraw[2], kpar[2], vraw[2];
;     kpar[0] = (u32x4){0u, 0u, 0u, 0u}; kpar[1] = kpar[0];
;     int tt = isctx ? 3 : (nb == 0 ? 1 : 0);
;     AT_PREFETCH(tt);
;     ...
;             LAS bf16* vt = (LAS bf16*)(C.lds + VT_OFF + (8 * cd) * VS + key * 2);
;     ...
;                     const LAS unsigned char* vp = C.lds + VT_OFF + (32 * db + r32) * VS + (32 * sub + 16 * s2 + 4 * h) * 2;
	global_load_dwordx4 v[138:141], v[18:19], off offset:2048
	global_load_dwordx4 v[142:145], v[18:19], off offset:2304
	v_add_u32_e32 v18, 0x200, v178
	v_ashrrev_i32_e32 v179, 3, v18
	v_bitop3_b32 v164, v28, 16, 56 bitop3:0x6c
	v_add_u32_e32 v18, v179, v25
	v_lshlrev_b32_e32 v20, 1, v164
	v_mov_b32_e32 v21, v3
	v_mad_i64_i32 v[18:19], s[6:7], v18, s66, v[44:45]
	v_lshl_add_u64 v[14:15], v[14:15], 0, v[20:21]
	v_lshl_add_u64 v[18:19], v[18:19], 0, s[38:39]
	v_lshl_add_u64 v[16:17], v[18:19], 0, v[16:17]
	global_load_dwordx4 v[126:129], v[14:15], off offset:2048
	global_load_dwordx4 v[146:149], v[16:17], off offset:2048
	v_lshl_add_u64 v[14:15], v[18:19], 0, v[20:21]
	global_load_dwordx4 v[130:133], v[14:15], off offset:2048
	global_load_dwordx4 v[150:153], v[16:17], off offset:2304
	v_lshlrev_b32_e32 v14, 16, v39
	v_and_b32_e32 v15, 0xffff0000, v39
	v_mov_b32_e32 v16, v26
	v_mov_b32_e32 v17, v4
	v_lshlrev_b32_e32 v12, 16, v43
	v_and_b32_e32 v13, 0xffff0000, v43
	v_pk_mul_f32 v[18:19], v[16:17], v[14:15]
	v_mov_b32_e32 v4, v27
	v_pk_fma_f32 v[18:19], v[4:5], v[12:13], v[18:19]
	v_pk_mul_f32 v[4:5], v[4:5], v[14:15]
	v_cvt_pk_bf16_f32 v134, v6, v7
	v_pk_fma_f32 v[4:5], v[16:17], v[12:13], v[4:5] neg_lo:[0,0,1] neg_hi:[0,0,1]
	v_and_b32_e32 v6, 4, v178
	v_pk_mul_f32 v[4:5], v[4:5], s[42:43] op_sel_hi:[1,0]
	v_cmp_eq_u32_e64 s[6:7], 0, v6
	v_cvt_pk_bf16_f32 v125, v4, v5
	v_pk_mul_f32 v[4:5], v[18:19], s[42:43] op_sel_hi:[1,0]
	v_and_b32_e32 v6, 2, v178
	v_cvt_pk_bf16_f32 v137, v4, v5
	v_mul_u32_u24_e32 v4, 0x108, v48
	v_add_u32_e32 v4, v4, v49
	v_add_u32_e32 v183, s78, v4
	v_or_b32_e32 v4, s58, v48
	v_sub_u32_e32 v4, v4, v180
	v_and_b32_e32 v5, 7, v178
	s_movk_i32 s26, 0x880
	v_add_u32_e32 v184, 4, v4
	v_mul_u32_u24_e32 v4, 0x90, v48
	s_lshl_b32 s34, s9, 1
	s_sub_i32 s51, 32, s8
	v_cmp_eq_u32_e64 s[8:9], 0, v6
	v_mul_lo_u32 v6, v159, s76
	v_lshlrev_b32_e32 v19, 4, v5
	v_mul_u32_u24_e32 v20, 0x840, v5
	v_mul_lo_u32 v5, v179, s76
	v_add3_u32 v185, v4, v2, 0
	v_sub_u32_e32 v2, v180, v48
	v_readfirstlane_b32 s18, v23
	s_addk_i32 s19, 0x3e80
	s_or_b32 s35, s34, 1
	v_add_u32_e32 v18, 0, v6
	v_lshlrev_b32_e32 v21, 1, v159
	v_lshlrev_b32_e32 v23, 1, v179
	v_subrev_u32_e32 v2, s58, v2
	v_mov_b32_e32 v16, v3
	v_mov_b32_e32 v17, v3
	v_cvt_pk_bf16_f32 v111, v64, v65
	v_cvt_pk_bf16_f32 v135, v8, v9
	v_cvt_pk_bf16_f32 v136, v10, v11
	v_readfirstlane_b32 s62, v24
	s_waitcnt vmcnt(6)
	v_mul_f32_e32 v192, 0x3fb8aa3b, v22
	v_add_u32_e32 v22, 0, v5
	v_and_b32_e32 v182, 8, v28
	s_add_u32 s56, s10, s38
	v_subrev_u32_e32 v186, 31, v2
	v_mov_b32_e32 v2, v3
	v_mov_b32_e32 v4, v3
	v_mov_b32_e32 v5, v3
	v_mov_b32_e32 v6, v3
	v_mov_b32_e32 v7, v3
	v_mov_b32_e32 v8, v3
	v_mov_b32_e32 v9, v3
	v_mov_b32_e32 v10, v3
	v_mov_b32_e32 v11, v3
	v_mov_b32_e32 v12, v3
	v_mov_b32_e32 v13, v3
	v_mov_b32_e32 v14, v3
	v_mov_b32_e32 v15, v3
	v_add_u32_e32 v187, v18, v19
	v_add_u32_e32 v188, v20, v21
	v_add_u32_e32 v189, v22, v19
	v_add_u32_e32 v190, v20, v23
	v_mov_b64_e32 v[32:33], v[16:17]
	v_mov_b64_e32 v[64:65], v[16:17]
	v_mov_b64_e32 v[48:49], v[16:17]
	v_mov_b64_e32 v[80:81], v[16:17]
	v_and_b32_e32 v178, 63, v179
	s_addc_u32 s57, s11, 0
	v_mov_b32_e32 v194, v192
	v_mov_b64_e32 v[30:31], v[14:15]
	v_mov_b64_e32 v[28:29], v[12:13]
	v_mov_b64_e32 v[26:27], v[10:11]
	v_mov_b64_e32 v[24:25], v[8:9]
	v_mov_b64_e32 v[22:23], v[6:7]
	v_mov_b64_e32 v[20:21], v[4:5]
	v_mov_b64_e32 v[18:19], v[2:3]
	v_mov_b64_e32 v[62:63], v[14:15]
	v_mov_b64_e32 v[60:61], v[12:13]
	v_mov_b64_e32 v[58:59], v[10:11]
	v_mov_b64_e32 v[56:57], v[8:9]
	v_mov_b64_e32 v[54:55], v[6:7]
	v_mov_b64_e32 v[52:53], v[4:5]
	v_mov_b64_e32 v[50:51], v[2:3]
	v_mov_b64_e32 v[46:47], v[14:15]
	v_mov_b64_e32 v[44:45], v[12:13]
	v_mov_b64_e32 v[42:43], v[10:11]
	v_mov_b64_e32 v[40:41], v[8:9]
	v_mov_b64_e32 v[38:39], v[6:7]
	v_mov_b64_e32 v[36:37], v[4:5]
	v_mov_b64_e32 v[34:35], v[2:3]
	v_mov_b64_e32 v[78:79], v[14:15]
	v_mov_b64_e32 v[76:77], v[12:13]
	v_mov_b64_e32 v[74:75], v[10:11]
	v_mov_b64_e32 v[72:73], v[8:9]
	v_mov_b64_e32 v[70:71], v[6:7]
	v_mov_b64_e32 v[68:69], v[4:5]
	v_mov_b64_e32 v[66:67], v[2:3]

; #define LAS __attribute__((address_space(3)))
; #define LDS_WAIT() asm volatile("s_waitcnt lgkmcnt(0)" ::: "memory")
; __device__ __forceinline__ void cvt8(const u32x4 r, float (&f)[8]) { f[0] = bflo(r.x); f[1] = bfhi(r.x); f[2] = bflo(r.y); f[3] = bfhi(r.y); f[4] = bflo(r.z); f[5] = bfhi(r.z); f[6] = bflo(r.w); f[7] = bfhi(r.w); }
; __device__ __forceinline__ bf16x8 pack8(const float (&f)[8]) { u32x4 w; w.x = pk2(f[0], f[1]); w.y = pk2(f[2], f[3]); w.z = pk2(f[4], f[5]); w.w = pk2(f[6], f[7]); return __builtin_bit_cast(bf16x8, w); }
; __device__ __forceinline__ void attn_unit(Ctx& C, int l, int uidx) {
;     ...
;         LDS_WAIT(); __builtin_amdgcn_s_barrier(); asm volatile("" ::: "memory");
; #pragma unroll
;         for (int r = 0; r < 2; ++r) {
;             const int idx = C.tid + 512 * r, key = idx >> 3, cd = idx & 7;
;             u32x4 raw = kraw[r];
;             if (band) {
;                 float x[8], y[8]; cvt8(raw, x); cvt8(kpar[r], y);
;                 const int tk = 128 * kb + key, pos = (cd & 4) ? (tk & 63) : (tk >> 6), i0 = 8 * (cd & 1); const bool isb = (cd >> 1) & 1;
; #pragma unroll
;                 for (int j = 0; j < 8; ++j) { const f32x2 cs = ROPE[pos * 16 + i0 + j]; x[j] = isb ? (x[j] * cs.x + y[j] * cs.y) : (x[j] * cs.x - y[j] * cs.y); }
;                 raw = __builtin_bit_cast(u32x4, pack8(x));
;             }
;             *(LAS u32x4*)(C.lds + key * KS + cd * 16) = raw;
;             const u32x4 vr = vraw[r];
;             LAS bf16* vt = (LAS bf16*)(C.lds + VT_OFF + (8 * cd) * VS + key * 2);
;             vt[0] = (bf16)(vr.x & 0xffff); vt[VS / 2] = (bf16)(vr.x >> 16); vt[2 * (VS / 2)] = (bf16)(vr.y & 0xffff); vt[3 * (VS / 2)] = (bf16)(vr.y >> 16);
;             vt[4 * (VS / 2)] = (bf16)(vr.z & 0xffff); vt[5 * (VS / 2)] = (bf16)(vr.z >> 16); vt[6 * (VS / 2)] = (bf16)(vr.w & 0xffff); vt[7 * (VS / 2)] = (bf16)(vr.w >> 16);
;         }
;         if (ntt < 5) AT_PREFETCH(ntt);
.LBB0_580:
	ds_write_b128 v187, v[4:7]
	s_waitcnt vmcnt(2)
	ds_write_b16 v188, v142 offset:18432
	ds_write_b16_d16_hi v188, v142 offset:18696
	ds_write_b16 v188, v143 offset:18960
	ds_write_b16_d16_hi v188, v143 offset:19224
	ds_write_b16 v188, v144 offset:19488
	ds_write_b16_d16_hi v188, v144 offset:19752
	ds_write_b16 v188, v145 offset:20016
	ds_write_b16_d16_hi v188, v145 offset:20280
	s_waitcnt vmcnt(1)
	v_mov_b64_e32 v[4:5], v[146:147]
	s_andn2_b64 vcc, exec, s[10:11]
	v_mov_b64_e32 v[6:7], v[148:149]
	s_cbranch_vccnz .LBB0_582
	v_add_u32_e32 v2, s26, v179
	v_ashrrev_i32_e32 v2, 6, v2
	v_cndmask_b32_e64 v2, v178, v2, s[6:7]
	v_lshl_or_b32 v4, v2, 4, v182
	v_ashrrev_i32_e32 v5, 31, v4
	v_lshl_add_u64 v[16:17], v[4:5], 3, s[14:15]
	global_load_dwordx4 v[4:7], v[16:17], off
	global_load_dwordx4 v[8:11], v[16:17], off offset:16
	global_load_dwordx4 v[12:15], v[16:17], off offset:32
	global_load_dwordx4 v[82:85], v[16:17], off offset:48
	s_waitcnt vmcnt(5)
	v_lshlrev_b32_e32 v91, 16, v130
	v_and_b32_e32 v92, 0xffff0000, v130
	v_lshlrev_b32_e32 v93, 16, v131
	v_and_b32_e32 v94, 0xffff0000, v131
	v_lshlrev_b32_e32 v95, 16, v132
	v_and_b32_e32 v96, 0xffff0000, v132
	v_lshlrev_b32_e32 v97, 16, v133
	v_and_b32_e32 v154, 0xffff0000, v133
	v_lshlrev_b32_e32 v2, 16, v146
	v_and_b32_e32 v16, 0xffff0000, v146
	v_lshlrev_b32_e32 v17, 16, v147
	v_and_b32_e32 v86, 0xffff0000, v147
	v_lshlrev_b32_e32 v87, 16, v148
	v_and_b32_e32 v88, 0xffff0000, v148
	v_lshlrev_b32_e32 v89, 16, v149
	v_and_b32_e32 v90, 0xffff0000, v149
	s_waitcnt vmcnt(3)
	v_mul_f32_e32 v5, v5, v91
	v_mul_f32_e32 v7, v7, v92
	s_waitcnt vmcnt(2)
	v_mul_f32_e32 v9, v9, v93
	v_mul_f32_e32 v11, v11, v94
	s_waitcnt vmcnt(1)
	v_mul_f32_e32 v13, v13, v95
	v_mul_f32_e32 v15, v15, v96
	s_waitcnt vmcnt(0)
	v_mul_f32_e32 v83, v83, v97
	v_mul_f32_e32 v85, v85, v154
	v_cndmask_b32_e64 v5, v5, -v5, s[8:9]
	v_cndmask_b32_e64 v7, v7, -v7, s[8:9]
	v_cndmask_b32_e64 v9, v9, -v9, s[8:9]
	v_cndmask_b32_e64 v11, v11, -v11, s[8:9]
	v_cndmask_b32_e64 v13, v13, -v13, s[8:9]
	v_cndmask_b32_e64 v15, v15, -v15, s[8:9]
	v_cndmask_b32_e64 v83, v83, -v83, s[8:9]
	v_cndmask_b32_e64 v85, v85, -v85, s[8:9]
	v_fmac_f32_e32 v5, v4, v2
	v_fmac_f32_e32 v7, v6, v16
	v_fmac_f32_e32 v9, v8, v17
	v_fmac_f32_e32 v11, v10, v86
	v_fmac_f32_e32 v13, v12, v87
	v_fmac_f32_e32 v15, v14, v88
	v_fmac_f32_e32 v83, v82, v89
	v_fmac_f32_e32 v85, v84, v90
	v_cvt_pk_bf16_f32 v4, v5, v7
	v_cvt_pk_bf16_f32 v5, v9, v11
	v_cvt_pk_bf16_f32 v6, v13, v15
	v_cvt_pk_bf16_f32 v7, v83, v85
.LBB0_582:
	s_cmp_gt_i32 s62, 1
	s_cselect_b64 s[10:11], -1, 0
	s_cmp_lt_u32 s62, s51
	s_cselect_b64 s[26:27], -1, 0
	s_or_b64 s[10:11], s[10:11], s[26:27]
	s_add_i32 s26, s62, 1
	s_and_b64 s[10:11], s[10:11], exec
	s_cselect_b32 s38, s26, 3
	s_cmp_gt_i32 s38, 4
	s_cselect_b64 s[58:59], -1, 0
	s_and_b64 vcc, exec, s[58:59]
	ds_write_b128 v189, v[4:7]
	s_waitcnt vmcnt(0)
	ds_write_b16 v190, v150 offset:18432
	ds_write_b16_d16_hi v190, v150 offset:18696
	ds_write_b16 v190, v151 offset:18960
	ds_write_b16_d16_hi v190, v151 offset:19224
	ds_write_b16 v190, v152 offset:19488
	ds_write_b16_d16_hi v190, v152 offset:19752
	ds_write_b16 v190, v153 offset:20016
	ds_write_b16_d16_hi v190, v153 offset:20280
	s_cbranch_vccnz .LBB0_592
	s_cmp_lt_i32 s38, 3
	s_cselect_b64 s[60:61], -1, 0
	s_cmp_gt_i32 s38, 2
	s_mov_b64 s[10:11], -1
	s_cbranch_scc0 .LBB0_585
	s_lshl_b32 s10, s38, 7
	s_add_i32 s26, s19, s10
	s_mov_b64 s[10:11], 0

; #define LAS __attribute__((address_space(3)))
; __device__ __forceinline__ float xor32_sum(float x) { const auto r = __builtin_amdgcn_permlane32_swap(__float_as_uint(x), __float_as_uint(x), false, false); return __uint_as_float(r[0]) + __uint_as_float(r[1]); }
; __device__ __forceinline__ float xor32_max(float x) { const auto r = __builtin_amdgcn_permlane32_swap(__float_as_uint(x), __float_as_uint(x), false, false); return fmaxf(__uint_as_float(r[0]), __uint_as_float(r[1])); }
; #define MFMA32(a, b, c) __builtin_amdgcn_mfma_f32_32x32x16_bf16((a), (b), (c), 0, 0, 0)
; __device__ __forceinline__ void attn_unit(Ctx& C, int l, int uidx) {
;     ...
;                 float mx = -INFINITY;
; #pragma unroll
;                 for (int i = 0; i < 16; ++i) { float x = S[i];
;                     if (tt == 0 || tt == 2) { const int kpos = 128 * kb + 32 * sub + (i & 3) + 8 * (i >> 2) + 4 * h; const int dq = tq - kpos; if (dq > 128 || dq < -128) x = -INFINITY; }
;                     S[i] = x; mx = fmaxf(mx, x); }
;                 mx = xor32_max(mx);
;                 const float mnew = fmaxf(m_[qb], mx), alpha = __builtin_amdgcn_exp2f(m_[qb] - mnew);
;                 float rs = 0.f; float p[16];
; #pragma unroll
;                 for (int i = 0; i < 16; ++i) { p[i] = __builtin_amdgcn_exp2f(S[i] - mnew); rs += p[i]; }
;                 rs = xor32_sum(rs);
;                 l_[qb] = l_[qb] * alpha + rs; m_[qb] = mnew;
; #pragma unroll
;                 for (int i = 0; i < 16; ++i) { O[0][qb][i] *= alpha; O[1][qb][i] *= alpha; }
; #pragma unroll
;                 for (int s2 = 0; s2 < 2; ++s2) { float t8[8];
; #pragma unroll
;                     for (int j = 0; j < 8; ++j) t8[j] = p[8 * s2 + j];
;                     Pf[qb][s2] = pack8(t8); }
;             }
; #pragma unroll
;             for (int db = 0; db < 2; ++db)
; #pragma unroll
;                 for (int s2 = 0; s2 < 2; ++s2) {
;                     const LAS unsigned char* vp = C.lds + VT_OFF + (32 * db + r32) * VS + (32 * sub + 16 * s2 + 4 * h) * 2;
;                     const u32x2 v0 = *(const LAS u32x2*)vp, v1 = *(const LAS u32x2*)(vp + 16);
;                     const u32x4 vv = {v0.x, v0.y, v1.x, v1.y}; const bf16x8 Vf = __builtin_bit_cast(bf16x8, vv);
;                     O[db][0] = MFMA32(Vf, Pf[0][s2], O[db][0]); O[db][1] = MFMA32(Vf, Pf[1][s2], O[db][1]);
;                 }
.Lattn_l0_nomask2:
.LBB0_756:
	v_max3_f32 v4, v82, s79, v83
	v_max3_f32 v4, v4, v84, v85
	v_max3_f32 v4, v4, v86, v87
	v_max3_f32 v4, v4, v88, v89
	v_max3_f32 v4, v4, v90, v91
	v_max3_f32 v4, v4, v92, v93
	v_max3_f32 v12, v4, v94, v95
	v_max3_f32 v12, v12, v96, v97
	v_mov_b32_e32 v13, v12
	s_nop 1
	v_permlane32_swap_b32_e32 v12, v13
	v_max3_f32 v155, v192, v12, v13
	v_sub_f32_e32 v13, v82, v155
	v_exp_f32_e32 v13, v13
	v_sub_f32_e32 v15, v83, v155
	v_exp_f32_e32 v15, v15
	v_sub_f32_e32 v82, v84, v155
	v_exp_f32_e32 v83, v82
	v_sub_f32_e32 v82, v85, v155
	v_exp_f32_e32 v84, v82
	v_sub_f32_e32 v82, v86, v155
	v_add_f32_e32 v14, 0, v13
	v_exp_f32_e32 v85, v82
	v_sub_f32_e32 v82, v87, v155
	v_add_f32_e32 v14, v15, v14
	v_exp_f32_e32 v87, v82
	v_sub_f32_e32 v82, v88, v155
	v_add_f32_e32 v14, v83, v14
	v_exp_f32_e32 v88, v82
	v_sub_f32_e32 v82, v89, v155
	v_add_f32_e32 v14, v84, v14
	v_exp_f32_e32 v89, v82
	v_sub_f32_e32 v82, v90, v155
	v_add_f32_e32 v14, v85, v14
	v_exp_f32_e32 v90, v82
	v_sub_f32_e32 v82, v91, v155
	v_add_f32_e32 v14, v87, v14
	v_exp_f32_e32 v91, v82
	v_sub_f32_e32 v82, v92, v155
	v_add_f32_e32 v14, v88, v14
	v_exp_f32_e32 v92, v82
	v_sub_f32_e32 v82, v93, v155
	v_add_f32_e32 v14, v89, v14
	v_exp_f32_e32 v93, v82
	v_sub_f32_e32 v82, v94, v155
	v_add_f32_e32 v14, v90, v14
	v_exp_f32_e32 v94, v82
	v_sub_f32_e32 v82, v95, v155
	v_add_f32_e32 v14, v91, v14
	v_exp_f32_e32 v95, v82
	v_sub_f32_e32 v82, v96, v155
	v_add_f32_e32 v14, v92, v14
	v_exp_f32_e32 v96, v82
	v_sub_f32_e32 v82, v97, v155
	v_add_f32_e32 v14, v93, v14
	v_exp_f32_e32 v97, v82
	v_add_f32_e32 v14, v94, v14
	v_add_f32_e32 v14, v95, v14
	v_sub_f32_e32 v12, v192, v155
	v_add_f32_e32 v14, v96, v14
	v_add_f32_e32 v14, v97, v14
	v_exp_f32_e32 v12, v12
	v_mov_b32_e32 v82, v14
	v_sub_f32_e32 v4, v194, v195
	s_nop 0
	v_permlane32_swap_b32_e32 v14, v82
	v_exp_f32_e32 v4, v4
	v_add_f32_e32 v86, v14, v82
	v_fmac_f32_e32 v86, v191, v12
	v_pk_mul_f32 v[48:49], v[48:49], v[12:13] op_sel_hi:[1,0]
	v_pk_mul_f32 v[46:47], v[46:47], v[12:13] op_sel_hi:[1,0]
	v_pk_mul_f32 v[44:45], v[44:45], v[12:13] op_sel_hi:[1,0]
	v_pk_mul_f32 v[42:43], v[42:43], v[12:13] op_sel_hi:[1,0]
	v_pk_mul_f32 v[40:41], v[40:41], v[12:13] op_sel_hi:[1,0]
	v_pk_mul_f32 v[38:39], v[38:39], v[12:13] op_sel_hi:[1,0]
	v_pk_mul_f32 v[36:37], v[36:37], v[12:13] op_sel_hi:[1,0]
	v_pk_mul_f32 v[34:35], v[34:35], v[12:13] op_sel_hi:[1,0]
	v_pk_mul_f32 v[32:33], v[32:33], v[12:13] op_sel_hi:[1,0]
	v_pk_mul_f32 v[30:31], v[30:31], v[12:13] op_sel_hi:[1,0]
	v_pk_mul_f32 v[28:29], v[28:29], v[12:13] op_sel_hi:[1,0]
	v_pk_mul_f32 v[26:27], v[26:27], v[12:13] op_sel_hi:[1,0]
	v_pk_mul_f32 v[24:25], v[24:25], v[12:13] op_sel_hi:[1,0]
	v_pk_mul_f32 v[22:23], v[22:23], v[12:13] op_sel_hi:[1,0]
	v_pk_mul_f32 v[20:21], v[20:21], v[12:13] op_sel_hi:[1,0]
	v_pk_mul_f32 v[18:19], v[18:19], v[12:13] op_sel_hi:[1,0]
	v_cvt_pk_bf16_f32 v82, v13, v15
	v_cvt_pk_bf16_f32 v83, v83, v84
	v_cvt_pk_bf16_f32 v84, v85, v87
	v_cvt_pk_bf16_f32 v85, v88, v89
	v_cvt_pk_bf16_f32 v12, v90, v91
	v_cvt_pk_bf16_f32 v13, v92, v93
	v_cvt_pk_bf16_f32 v14, v94, v95
	ds_read2_b64 v[88:91], v2 offset1:2
	ds_read2_b64 v[92:95], v2 offset0:4 offset1:6
	v_pk_mul_f32 v[80:81], v[80:81], v[4:5] op_sel_hi:[1,0]
	v_pk_mul_f32 v[78:79], v[78:79], v[4:5] op_sel_hi:[1,0]
	v_pk_mul_f32 v[76:77], v[76:77], v[4:5] op_sel_hi:[1,0]
	v_pk_mul_f32 v[74:75], v[74:75], v[4:5] op_sel_hi:[1,0]
	v_pk_mul_f32 v[72:73], v[72:73], v[4:5] op_sel_hi:[1,0]
	v_pk_mul_f32 v[70:71], v[70:71], v[4:5] op_sel_hi:[1,0]
	v_pk_mul_f32 v[68:69], v[68:69], v[4:5] op_sel_hi:[1,0]
	v_pk_mul_f32 v[66:67], v[66:67], v[4:5] op_sel_hi:[1,0]
	v_cvt_pk_bf16_f32 v8, v199, v200
	v_cvt_pk_bf16_f32 v9, v201, v202
	v_cvt_pk_bf16_f32 v10, v203, v204
	v_cvt_pk_bf16_f32 v11, v205, v206
	v_add_u32_e32 v87, 0x2000, v2
	s_waitcnt lgkmcnt(1)
	v_mfma_f32_32x32x16_bf16 v[34:49], v[88:91], v[82:85], v[34:49]
	v_mul_f32_e64 v64, v64, v4
	v_mul_f32_e64 v65, v65, v4
	v_mul_f32_e64 v62, v62, v4
	v_mul_f32_e64 v63, v63, v4
	v_mul_f32_e64 v60, v60, v4
	v_mul_f32_e64 v61, v61, v4
	v_pk_mul_f32 v[58:59], v[58:59], v[4:5] op_sel_hi:[1,0]
	v_pk_mul_f32 v[56:57], v[56:57], v[4:5] op_sel_hi:[1,0]
	v_pk_mul_f32 v[54:55], v[54:55], v[4:5] op_sel_hi:[1,0]
	v_pk_mul_f32 v[52:53], v[52:53], v[4:5] op_sel_hi:[1,0]
	v_mfma_f32_32x32x16_bf16 v[66:81], v[88:91], v[8:11], v[66:81]
	ds_read2_b64 v[88:91], v87 offset0:32 offset1:34
	v_mul_f32_e64 v50, v50, v4
	v_mul_f32_e64 v51, v51, v4
	v_add_f32_e32 v154, v215, v216
	v_fmac_f32_e32 v154, v193, v4
	v_cvt_pk_bf16_f32 v4, v207, v208
	v_cvt_pk_bf16_f32 v5, v209, v210
	v_cvt_pk_bf16_f32 v6, v211, v212
	s_waitcnt lgkmcnt(0)
	v_mfma_f32_32x32x16_bf16 v[50:65], v[88:91], v[8:11], v[50:65]
	ds_read2_b64 v[8:11], v87 offset0:36 offset1:38
	v_cvt_pk_bf16_f32 v7, v213, v214
	v_cvt_pk_bf16_f32 v15, v96, v97
	s_add_i32 s64, s64, 1
	v_add_u32_e32 v2, 64, v2
	v_add_u32_e32 v16, 0x1200, v16
	s_cmp_ge_u32 s64, s63
	v_mfma_f32_32x32x16_bf16 v[18:33], v[88:91], v[82:85], v[18:33]
	v_mfma_f32_32x32x16_bf16 v[66:81], v[92:95], v[4:7], v[66:81]
	v_mfma_f32_32x32x16_bf16 v[34:49], v[92:95], v[12:15], v[34:49]
	s_waitcnt lgkmcnt(0)
	v_mfma_f32_32x32x16_bf16 v[50:65], v[8:11], v[4:7], v[50:65]
	v_mfma_f32_32x32x16_bf16 v[18:33], v[8:11], v[12:15], v[18:33]
	s_cbranch_scc1 .LBB0_789
	v_mov_b32_e32 v198, v17
	v_mov_b32_e32 v197, v196
	v_mov_b32_e32 v192, v155
	v_mov_b32_e32 v194, v195
	v_mov_b32_e32 v191, v86
	v_mov_b32_e32 v193, v154
	s_branch .LBB0_594

; #define LAS __attribute__((address_space(3)))
; __device__ __forceinline__ void cvt8(const u32x4 r, float (&f)[8]) { f[0] = bflo(r.x); f[1] = bfhi(r.x); f[2] = bflo(r.y); f[3] = bfhi(r.y); f[4] = bflo(r.z); f[5] = bfhi(r.z); f[6] = bflo(r.w); f[7] = bfhi(r.w); }
; __device__ __forceinline__ void pool_unit(Ctx& C, int l, int blk) {
;     ...
;         for (int k = 0; k < 4; ++k) { const int tt = 4 * tg + k, t = t0 + tt; const int lo = max(t - hw, 0), hi = min(t + hw, L);
;             float sacc[8];
; #pragma unroll
;             for (int j = 0; j < 8; ++j) sacc[j] = 0.f;
;             for (int q = lo; q < hi; ++q) { float f[8]; cvt8(*(const LAS u32x4*)(C.lds + (q - t0 + 8) * RS + c8 * 16), f);
.LBB0_1726:
	v_or_b32_e32 v18, s18, v16
	v_add_u32_e32 v6, s11, v18
	v_sub_u32_e32 v7, v6, v5
	v_add_u32_e32 v6, v6, v5
	v_max_i32_e32 v19, 0, v7
	v_min_i32_e32 v20, 0x1000, v6
	v_mov_b32_e32 v9, 0
	v_cmp_gt_i32_e32 vcc, v20, v19
	v_mov_b32_e32 v8, v9
	v_mov_b32_e32 v11, v9
	v_mov_b32_e32 v10, v9
	v_mov_b32_e32 v13, v9
	v_mov_b32_e32 v12, v9
	v_mov_b32_e32 v7, v9
	v_mov_b32_e32 v6, v9
	s_and_saveexec_b64 s[6:7], vcc
	s_cbranch_execz .LBB0_1725
	v_max_i32_e32 v6, 0, v17
	v_mad_u64_u32 v[14:15], s[8:9], v6, s67, v[4:5]
	v_mov_b32_e32 v6, 0
	s_mov_b64 s[8:9], 0
	v_mov_b32_e32 v15, v19
	v_mov_b32_e32 v7, v6
	v_mov_b32_e32 v12, v6
	v_mov_b32_e32 v13, v6
	v_mov_b32_e32 v10, v6
	v_mov_b32_e32 v11, v6
	v_mov_b32_e32 v8, v6
	v_mov_b32_e32 v9, v6
	ds_read_b128 v[244:247], v14
	v_add_u32_e32 v14, 0x410, v14

; __device__ __forceinline__ void cvt8(const u32x4 r, float (&f)[8]) { f[0] = bflo(r.x); f[1] = bfhi(r.x); f[2] = bflo(r.y); f[3] = bfhi(r.y); f[4] = bflo(r.z); f[5] = bfhi(r.z); f[6] = bflo(r.w); f[7] = bfhi(r.w); }
; __device__ __forceinline__ bf16x8 pack8(const float (&f)[8]) { u32x4 w; w.x = pk2(f[0], f[1]); w.y = pk2(f[2], f[3]); w.z = pk2(f[4], f[5]); w.w = pk2(f[6], f[7]); return __builtin_bit_cast(bf16x8, w); }
; __device__ __forceinline__ void attn_unit(Ctx& C, int l, int uidx) {
;     ...
;     if (!isctx) { b = uidx >> 6; kh = (uidx >> 5) & 1; nb = uidx & 31; } else { const int v = uidx - 256; b = v >> 2; kh = (v >> 1) & 1; nb = v & 1; }
;     const int rowbase = isctx ? NLAT + b * CL : b * SL, crow = NLAT + b * CL;
;     const int g = C.wave >> 1, th = C.wave & 1, head = kh * 4 + g, r32 = C.lane & 31, h = C.lane >> 5;
;     const bf16* Z = WSP(bf16, WS_Z); const f32x2* ROPE = WSP(f32x2, WS_ROPE);
;     bf16x8 Qf[2][4];
; #pragma unroll
;     for (int qb = 0; qb < 2; ++qb) {
;         const int tq = 128 * nb + 64 * th + 32 * qb + r32;
;         const bf16* qp = Z + (size_t)(rowbase + tq) * INW + 512 + 64 * head + 8 * h;
;         float f[4][8];
; #pragma unroll
;         for (int s = 0; s < 4; ++s) cvt8(*(const u32x4*)(qp + 16 * s), f[s]);
;         if (!isctx) {
;             const int pr = tq >> 6, pc = tq & 63;
; #pragma unroll
;             for (int j = 0; j < 8; ++j) {
;                 const f32x2 cr = ROPE[pr * 16 + 8 * h + j], cc = ROPE[pc * 16 + 8 * h + j];
;                 const float a0 = f[0][j], b0 = f[1][j]; f[0][j] = a0 * cr.x - b0 * cr.y; f[1][j] = b0 * cr.x + a0 * cr.y;
;                 const float a1 = f[2][j], b1 = f[3][j]; f[2][j] = a1 * cc.x - b1 * cc.y; f[3][j] = b1 * cc.x + a1 * cc.y; }
;         }
; #pragma unroll
;         for (int s = 0; s < 4; ++s) {
; #pragma unroll
;             for (int j = 0; j < 8; ++j) f[s][j] *= 0.125f * LOG2E;
;             Qf[qb][s] = pack8(f[s]); }
;     }
.LBB0_1735:
	s_andn2_b64 vcc, exec, s[6:7]
	s_cbranch_vccnz .LBB0_1951
	s_ashr_i32 s6, s56, 6
	s_bfe_u32 s18, s56, 0x10005
	s_lshl_b32 s19, s6, 8
	s_lshl_b32 s59, s6, 12
	s_ashr_i32 s6, s57, 7
	s_lshl_b32 s7, s18, 2
	s_and_b32 s8, s56, 31
	s_bfe_u32 s9, s57, 0x10006
	s_add_i32 s6, s6, s7
	s_add_u32 s10, s46, 0x36000000
	s_addc_u32 s11, s47, 0
	s_add_u32 s52, s46, 0x200000
	s_addc_u32 s53, s47, 0
	s_lshl_b32 s7, s8, 7
	s_lshl_b32 s54, s9, 6
	v_and_b32_e32 v48, 31, v172
	s_or_b32 s7, s54, s7
	v_lshrrev_b32_e32 v50, 5, v160
	v_or_b32_e32 v51, s7, v48
	s_lshl_b32 s34, s6, 6
	v_lshlrev_b32_e32 v49, 3, v50
	s_lshr_b32 s7, s7, 2
	v_or_b32_e32 v160, s59, v51
	v_mov_b64_e32 v[44:45], s[10:11]
	v_or_b32_e32 v2, s7, v49
	s_ashr_i32 s35, s34, 31
	v_mad_i64_i32 v[20:21], s[50:51], v160, s63, v[44:45]
	v_lshlrev_b32_e32 v2, 3, v2
	s_lshl_b64 s[50:51], s[34:35], 1
	global_load_dwordx4 v[12:15], v2, s[52:53] offset:16
	global_load_dwordx4 v[16:19], v2, s[52:53]
	global_load_dwordx4 v[4:7], v2, s[52:53] offset:48
	global_load_dwordx4 v[8:11], v2, s[52:53] offset:32
	v_lshl_add_u64 v[20:21], v[20:21], 0, s[50:51]
	v_lshlrev_b32_e32 v2, 4, v50
	v_lshl_add_u64 v[20:21], v[20:21], 0, v[2:3]
	global_load_dwordx4 v[52:55], v[20:21], off offset:1024
	global_load_dwordx4 v[56:59], v[20:21], off offset:1056
	global_load_dwordx4 v[24:27], v[20:21], off offset:1088
	global_load_dwordx4 v[28:31], v[20:21], off offset:1120
	v_lshlrev_b32_e32 v22, 6, v50
	v_lshl_or_b32 v32, v48, 7, v22
	global_load_dwordx4 v[40:43], v32, s[52:53]
	global_load_dwordx4 v[36:39], v32, s[52:53] offset:16
	global_load_dwordx4 v[20:23], v32, s[52:53] offset:48
	s_nop 0
	global_load_dwordx4 v[32:35], v32, s[52:53] offset:32
	v_or_b32_e32 v51, 32, v51
	s_movk_i32 s7, 0x3f0
	v_ashrrev_i32_e32 v173, 3, v172
	v_lshlrev_b32_e32 v175, 2, v50
	v_ashrrev_i32_e32 v161, 31, v160
	v_and_b32_e32 v176, 63, v173
	v_mov_b32_e32 v186, 1.0
	v_mov_b32_e32 v189, 1.0
	s_waitcnt vmcnt(0)
	v_mov_b32_e32 v46, v16
	v_mov_b32_e32 v47, v18
	v_mov_b32_e32 v18, v17
	v_mov_b32_e32 v16, v12
	v_mov_b32_e32 v17, v14
	v_mov_b32_e32 v14, v13
	v_mov_b32_e32 v12, v8
	v_mov_b32_e32 v13, v10
	v_lshlrev_b32_e32 v60, 16, v56
	v_and_b32_e32 v61, 0xffff0000, v56
	v_lshlrev_b32_e32 v56, 16, v57
	v_and_b32_e32 v57, 0xffff0000, v57
	v_lshlrev_b32_e32 v64, 16, v58
	v_and_b32_e32 v65, 0xffff0000, v58
	v_mov_b32_e32 v10, v9
	v_mov_b32_e32 v8, v4
	v_mov_b32_e32 v9, v6
	v_mov_b32_e32 v6, v5
	v_lshlrev_b32_e32 v4, 16, v52
	v_and_b32_e32 v5, 0xffff0000, v52
	v_lshlrev_b32_e32 v52, 16, v53
	v_and_b32_e32 v53, 0xffff0000, v53
	v_lshlrev_b32_e32 v62, 16, v54
	v_and_b32_e32 v63, 0xffff0000, v54
	v_pk_mul_f32 v[66:67], v[46:47], v[60:61]
	v_pk_mul_f32 v[60:61], v[18:19], v[60:61]
	v_pk_mul_f32 v[68:69], v[16:17], v[56:57]
	v_pk_mul_f32 v[56:57], v[14:15], v[56:57]
	v_pk_mul_f32 v[70:71], v[12:13], v[64:65]
	v_pk_mul_f32 v[64:65], v[10:11], v[64:65]
	v_pk_fma_f32 v[66:67], v[18:19], v[4:5], v[66:67]
	v_pk_fma_f32 v[4:5], v[46:47], v[4:5], v[60:61] neg_lo:[0,0,1] neg_hi:[0,0,1]
	v_pk_fma_f32 v[60:61], v[14:15], v[52:53], v[68:69]
	v_pk_fma_f32 v[52:53], v[16:17], v[52:53], v[56:57] neg_lo:[0,0,1] neg_hi:[0,0,1]
	v_pk_fma_f32 v[56:57], v[10:11], v[62:63], v[70:71]
	v_pk_fma_f32 v[62:63], v[12:13], v[62:63], v[64:65] neg_lo:[0,0,1] neg_hi:[0,0,1]
	v_pk_mul_f32 v[64:65], v[66:67], s[38:39] op_sel_hi:[1,0]
	v_pk_mul_f32 v[66:67], v[56:57], s[38:39] op_sel_hi:[1,0]
	v_or_b32_e32 v56, s59, v51
	v_mad_i64_i32 v[56:57], s[34:35], v56, s63, v[44:45]
	v_lshlrev_b32_e32 v58, 16, v59
	v_and_b32_e32 v59, 0xffff0000, v59
	v_pk_mul_f32 v[52:53], v[52:53], s[38:39] op_sel_hi:[1,0]
	v_pk_mul_f32 v[62:63], v[62:63], s[38:39] op_sel_hi:[1,0]
	v_lshl_add_u64 v[56:57], v[56:57], 0, s[50:51]
	v_lshlrev_b32_e32 v54, 16, v55
	v_and_b32_e32 v55, 0xffff0000, v55
	v_pk_mul_f32 v[72:73], v[8:9], v[58:59]
	v_pk_mul_f32 v[4:5], v[4:5], s[38:39] op_sel_hi:[1,0]
	v_cvt_pk_bf16_f32 v105, v52, v53
	v_cvt_pk_bf16_f32 v106, v62, v63
	v_pk_mul_f32 v[52:53], v[6:7], v[58:59]
	v_lshl_add_u64 v[62:63], v[56:57], 0, v[2:3]
	v_cvt_pk_bf16_f32 v104, v4, v5
	v_pk_fma_f32 v[4:5], v[6:7], v[54:55], v[72:73]
	v_pk_fma_f32 v[68:69], v[8:9], v[54:55], v[52:53] neg_lo:[0,0,1] neg_hi:[0,0,1]
	global_load_dwordx4 v[52:55], v[62:63], off offset:1024
	global_load_dwordx4 v[56:59], v[62:63], off offset:1056
	v_pk_mul_f32 v[60:61], v[60:61], s[38:39] op_sel_hi:[1,0]
	v_pk_mul_f32 v[4:5], v[4:5], s[38:39] op_sel_hi:[1,0]
	v_cvt_pk_bf16_f32 v108, v64, v65
	v_cvt_pk_bf16_f32 v109, v60, v61
	v_lshlrev_b32_e32 v60, 16, v28
	v_and_b32_e32 v61, 0xffff0000, v28
	v_mov_b32_e32 v64, v40
	v_mov_b32_e32 v65, v42
	v_cvt_pk_bf16_f32 v110, v66, v67
	v_cvt_pk_bf16_f32 v111, v4, v5
	v_lshlrev_b32_e32 v4, 16, v24
	v_and_b32_e32 v5, 0xffff0000, v24
	v_pk_mul_f32 v[66:67], v[64:65], v[60:61]
	v_mov_b32_e32 v42, v41
	v_pk_fma_f32 v[40:41], v[42:43], v[4:5], v[66:67]
	v_pk_mul_f32 v[42:43], v[42:43], v[60:61]
	v_lshlrev_b32_e32 v28, 16, v29
	v_pk_fma_f32 v[4:5], v[64:65], v[4:5], v[42:43] neg_lo:[0,0,1] neg_hi:[0,0,1]
	v_and_b32_e32 v29, 0xffff0000, v29
	v_pk_mul_f32 v[4:5], v[4:5], s[38:39] op_sel_hi:[1,0]
	v_lshlrev_b32_e32 v24, 16, v25
	v_cvt_pk_bf16_f32 v112, v4, v5
	v_pk_mul_f32 v[4:5], v[40:41], s[38:39] op_sel_hi:[1,0]
	v_mov_b32_e32 v40, v36
	v_mov_b32_e32 v41, v38
	v_mov_b32_e32 v38, v37
	v_and_b32_e32 v25, 0xffff0000, v25
	v_pk_mul_f32 v[42:43], v[40:41], v[28:29]
	v_pk_mul_f32 v[28:29], v[38:39], v[28:29]
	v_pk_fma_f32 v[36:37], v[38:39], v[24:25], v[42:43]
	v_pk_fma_f32 v[24:25], v[40:41], v[24:25], v[28:29] neg_lo:[0,0,1] neg_hi:[0,0,1]
	v_lshlrev_b32_e32 v28, 16, v30
	v_pk_mul_f32 v[24:25], v[24:25], s[38:39] op_sel_hi:[1,0]
; __device__ __forceinline__ void cvt8(const u32x4 r, float (&f)[8]) { f[0] = bflo(r.x); f[1] = bfhi(r.x); f[2] = bflo(r.y); f[3] = bfhi(r.y); f[4] = bflo(r.z); f[5] = bfhi(r.z); f[6] = bflo(r.w); f[7] = bfhi(r.w); }
; __device__ __forceinline__ bf16x8 pack8(const float (&f)[8]) { u32x4 w; w.x = pk2(f[0], f[1]); w.y = pk2(f[2], f[3]); w.z = pk2(f[4], f[5]); w.w = pk2(f[6], f[7]); return __builtin_bit_cast(bf16x8, w); }
; __device__ __forceinline__ void attn_unit(Ctx& C, int l, int uidx) {
;     ...
;     for (int qb = 0; qb < 2; ++qb) {
;         const int tq = 128 * nb + 64 * th + 32 * qb + r32;
;         const bf16* qp = Z + (size_t)(rowbase + tq) * INW + 512 + 64 * head + 8 * h;
;         float f[4][8];
; #pragma unroll
;         for (int s = 0; s < 4; ++s) cvt8(*(const u32x4*)(qp + 16 * s), f[s]);
;         if (!isctx) {
;             const int pr = tq >> 6, pc = tq & 63;
; #pragma unroll
;             for (int j = 0; j < 8; ++j) {
;                 const f32x2 cr = ROPE[pr * 16 + 8 * h + j], cc = ROPE[pc * 16 + 8 * h + j];
;                 const float a0 = f[0][j], b0 = f[1][j]; f[0][j] = a0 * cr.x - b0 * cr.y; f[1][j] = b0 * cr.x + a0 * cr.y;
;                 const float a1 = f[2][j], b1 = f[3][j]; f[2][j] = a1 * cc.x - b1 * cc.y; f[3][j] = b1 * cc.x + a1 * cc.y; }
;         }
; #pragma unroll
;         for (int s = 0; s < 4; ++s) {
; #pragma unroll
;             for (int j = 0; j < 8; ++j) f[s][j] *= 0.125f * LOG2E;
;             Qf[qb][s] = pack8(f[s]); }
;     }
;     float m_[2], l_[2]; f32x16 O[2][2];
;     { const float sk = INP(I_SINK)[l * 8 + head] * LOG2E; m_[0] = sk; m_[1] = sk; l_[0] = 1.f; l_[1] = 1.f; }
; #pragma unroll
;     for (int a = 0; a < 2; ++a)
; #pragma unroll
;         for (int q = 0; q < 2; ++q)
; #pragma unroll
;             for (int i = 0; i < 16; ++i) O[a][q][i] = 0.f;
;     ...
;     __syncthreads();
;     u32x4 kraw[2], kpar[2], vraw[2];
;     kpar[0] = (u32x4){0u, 0u, 0u, 0u}; kpar[1] = kpar[0];
;     int tt = isctx ? 3 : (nb == 0 ? 1 : 0);
;     AT_PREFETCH(tt);
	v_and_b32_e32 v29, 0xffff0000, v30
	v_cvt_pk_bf16_f32 v113, v24, v25
	v_lshlrev_b32_e32 v24, 16, v26
	v_and_b32_e32 v25, 0xffff0000, v26
	v_lshlrev_b32_e32 v26, 4, v51
	v_mov_b32_e32 v66, v32
	v_mov_b32_e32 v67, v34
	v_and_or_b32 v26, v26, s7, v49
	v_pk_mul_f32 v[68:69], v[68:69], s[38:39] op_sel_hi:[1,0]
	v_pk_mul_f32 v[64:65], v[36:37], s[38:39] op_sel_hi:[1,0]
	v_pk_mul_f32 v[36:37], v[66:67], v[28:29]
	v_mov_b32_e32 v34, v33
	v_lshlrev_b32_e32 v51, 3, v26
	v_cvt_pk_bf16_f32 v107, v68, v69
	v_pk_fma_f32 v[32:33], v[34:35], v[24:25], v[36:37]
	global_load_dwordx4 v[40:43], v[62:63], off offset:1088
	global_load_dwordx4 v[36:39], v[62:63], off offset:1120
	global_load_dwordx2 v[68:69], v51, s[52:53]
	s_nop 0
	global_load_dwordx4 v[60:63], v51, s[52:53] offset:8
	v_pk_mul_f32 v[28:29], v[34:35], v[28:29]
	v_lshlrev_b32_e32 v34, 16, v27
	v_pk_fma_f32 v[24:25], v[66:67], v[24:25], v[28:29] neg_lo:[0,0,1] neg_hi:[0,0,1]
	v_and_b32_e32 v35, 0xffff0000, v27
	v_pk_mul_f32 v[24:25], v[24:25], s[38:39] op_sel_hi:[1,0]
	v_lshlrev_b32_e32 v66, 16, v31
	v_cvt_pk_bf16_f32 v114, v24, v25
	v_and_b32_e32 v67, 0xffff0000, v31
	global_load_dwordx4 v[24:27], v51, s[52:53] offset:40
	global_load_dwordx4 v[28:31], v51, s[52:53] offset:24
	v_mov_b32_e32 v70, v20
	v_mov_b32_e32 v71, v22
	v_pk_mul_f32 v[72:73], v[70:71], v[66:67]
	v_mov_b32_e32 v22, v21
	v_pk_fma_f32 v[20:21], v[22:23], v[34:35], v[72:73]
	v_pk_mul_f32 v[22:23], v[22:23], v[66:67]
	v_pk_mul_f32 v[32:33], v[32:33], s[38:39] op_sel_hi:[1,0]
	v_pk_fma_f32 v[22:23], v[70:71], v[34:35], v[22:23] neg_lo:[0,0,1] neg_hi:[0,0,1]
	v_pk_mul_f32 v[20:21], v[20:21], s[38:39] op_sel_hi:[1,0]
	v_pk_mul_f32 v[22:23], v[22:23], s[38:39] op_sel_hi:[1,0]
	v_cvt_pk_bf16_f32 v118, v32, v33
	v_cvt_pk_bf16_f32 v115, v22, v23
	v_cvt_pk_bf16_f32 v119, v20, v21
	s_load_dwordx2 s[34:35], s[48:49], 0x58
	v_cvt_pk_bf16_f32 v116, v4, v5
	global_load_dwordx2 v[4:5], v51, s[52:53] offset:56
	s_ashr_i32 s7, s6, 31
	s_lshl_b64 s[6:7], s[6:7], 2
	s_waitcnt lgkmcnt(0)
	s_add_u32 s6, s34, s6
	s_waitcnt vmcnt(8)
	v_lshlrev_b32_e32 v20, 16, v52
	s_waitcnt vmcnt(7)
	v_lshlrev_b32_e32 v22, 16, v56
	v_and_b32_e32 v23, 0xffff0000, v56
	v_and_b32_e32 v21, 0xffff0000, v52
	v_pk_mul_f32 v[32:33], v[46:47], v[22:23]
	s_addc_u32 s7, s35, s7
	v_pk_fma_f32 v[32:33], v[18:19], v[20:21], v[32:33]
	v_pk_mul_f32 v[18:19], v[18:19], v[22:23]
	v_lshlrev_b32_e32 v22, 16, v57
	v_pk_fma_f32 v[18:19], v[46:47], v[20:21], v[18:19] neg_lo:[0,0,1] neg_hi:[0,0,1]
	v_and_b32_e32 v23, 0xffff0000, v57
	v_pk_mul_f32 v[18:19], v[18:19], s[38:39] op_sel_hi:[1,0]
	v_lshlrev_b32_e32 v20, 16, v53
	v_cvt_pk_bf16_f32 v120, v18, v19
	v_pk_mul_f32 v[18:19], v[32:33], s[38:39] op_sel_hi:[1,0]
	v_and_b32_e32 v21, 0xffff0000, v53
	v_pk_mul_f32 v[32:33], v[16:17], v[22:23]
	s_lshl_b32 s26, s18, 7
	v_pk_fma_f32 v[32:33], v[14:15], v[20:21], v[32:33]
	v_pk_mul_f32 v[14:15], v[14:15], v[22:23]
	v_cvt_pk_bf16_f32 v124, v18, v19
	v_pk_fma_f32 v[14:15], v[16:17], v[20:21], v[14:15] neg_lo:[0,0,1] neg_hi:[0,0,1]
	v_lshlrev_b32_e32 v20, 16, v58
	v_and_b32_e32 v21, 0xffff0000, v58
	v_lshlrev_b32_e32 v16, 16, v54
	v_and_b32_e32 v17, 0xffff0000, v54
	v_pk_mul_f32 v[22:23], v[12:13], v[20:21]
	v_pk_mul_f32 v[14:15], v[14:15], s[38:39] op_sel_hi:[1,0]
	v_pk_fma_f32 v[22:23], v[10:11], v[16:17], v[22:23]
	v_pk_mul_f32 v[10:11], v[10:11], v[20:21]
	v_cvt_pk_bf16_f32 v121, v14, v15
	v_pk_fma_f32 v[10:11], v[12:13], v[16:17], v[10:11] neg_lo:[0,0,1] neg_hi:[0,0,1]
	v_lshlrev_b32_e32 v16, 16, v59
	v_and_b32_e32 v17, 0xffff0000, v59
	v_lshlrev_b32_e32 v12, 16, v55
	v_and_b32_e32 v13, 0xffff0000, v55
	v_pk_mul_f32 v[20:21], v[8:9], v[16:17]
	v_pk_mul_f32 v[10:11], v[10:11], s[38:39] op_sel_hi:[1,0]
	v_pk_fma_f32 v[20:21], v[6:7], v[12:13], v[20:21]
	v_pk_mul_f32 v[6:7], v[6:7], v[16:17]
	v_cvt_pk_bf16_f32 v122, v10, v11
	v_pk_fma_f32 v[6:7], v[8:9], v[12:13], v[6:7] neg_lo:[0,0,1] neg_hi:[0,0,1]
	v_pk_mul_f32 v[10:11], v[22:23], s[38:39] op_sel_hi:[1,0]
	v_pk_mul_f32 v[6:7], v[6:7], s[38:39] op_sel_hi:[1,0]
	v_cvt_pk_bf16_f32 v126, v10, v11
	v_cvt_pk_bf16_f32 v123, v6, v7
	v_pk_mul_f32 v[6:7], v[20:21], s[38:39] op_sel_hi:[1,0]
	v_pk_mul_f32 v[14:15], v[32:33], s[38:39] op_sel_hi:[1,0]
	v_cvt_pk_bf16_f32 v127, v6, v7
	s_waitcnt vmcnt(6)
	v_lshlrev_b32_e32 v6, 16, v40
	s_waitcnt vmcnt(5)
	v_lshlrev_b32_e32 v8, 16, v36
	v_and_b32_e32 v9, 0xffff0000, v36
	s_waitcnt vmcnt(4)
	v_mov_b32_e32 v10, v68
	s_waitcnt vmcnt(3)
	v_mov_b32_e32 v11, v60
	v_mov_b32_e32 v60, v69
	v_and_b32_e32 v7, 0xffff0000, v40
	v_pk_mul_f32 v[12:13], v[10:11], v[8:9]
	v_pk_mul_f32 v[8:9], v[60:61], v[8:9]
	v_pk_fma_f32 v[12:13], v[60:61], v[6:7], v[12:13]
	v_pk_fma_f32 v[6:7], v[10:11], v[6:7], v[8:9] neg_lo:[0,0,1] neg_hi:[0,0,1]
	v_lshlrev_b32_e32 v10, 16, v37
	v_pk_mul_f32 v[6:7], v[6:7], s[38:39] op_sel_hi:[1,0]
	v_and_b32_e32 v11, 0xffff0000, v37
	v_cvt_pk_bf16_f32 v128, v6, v7
	v_pk_mul_f32 v[6:7], v[12:13], s[38:39] op_sel_hi:[1,0]
	v_mov_b32_e32 v12, v62
	s_waitcnt vmcnt(1)
	v_mov_b32_e32 v13, v28
	v_mov_b32_e32 v28, v63
	v_cvt_pk_bf16_f32 v125, v14, v15
	v_lshlrev_b32_e32 v8, 16, v41
	v_and_b32_e32 v9, 0xffff0000, v41
	v_pk_mul_f32 v[14:15], v[12:13], v[10:11]
	v_pk_mul_f32 v[10:11], v[28:29], v[10:11]
	v_pk_fma_f32 v[14:15], v[28:29], v[8:9], v[14:15]
	v_pk_fma_f32 v[8:9], v[12:13], v[8:9], v[10:11] neg_lo:[0,0,1] neg_hi:[0,0,1]
	v_lshlrev_b32_e32 v12, 16, v38
	v_pk_mul_f32 v[8:9], v[8:9], s[38:39] op_sel_hi:[1,0]
	v_and_b32_e32 v13, 0xffff0000, v38
	v_cvt_pk_bf16_f32 v129, v8, v9
	v_pk_mul_f32 v[8:9], v[14:15], s[38:39] op_sel_hi:[1,0]
	v_mov_b32_e32 v14, v30
	v_mov_b32_e32 v15, v24
	v_mov_b32_e32 v24, v31
	v_lshlrev_b32_e32 v10, 16, v42
	v_and_b32_e32 v11, 0xffff0000, v42
	v_pk_mul_f32 v[16:17], v[14:15], v[12:13]
	v_pk_mul_f32 v[12:13], v[24:25], v[12:13]
	v_sub_co_u32_e64 v23, vcc, s8, 1
	v_pk_fma_f32 v[16:17], v[24:25], v[10:11], v[16:17]
	v_pk_fma_f32 v[10:11], v[14:15], v[10:11], v[12:13] neg_lo:[0,0,1] neg_hi:[0,0,1]
	v_cndmask_b32_e64 v24, 0, 1, vcc
	v_addc_co_u32_e32 v14, vcc, 0, v23, vcc
	v_lshlrev_b32_e32 v14, 7, v14
	v_add_u32_e32 v25, s59, v14
	v_lshlrev_b32_e32 v28, 3, v172
	v_add_u32_e32 v14, v173, v25
	global_load_dword v22, v3, s[6:7] offset:32
	v_pk_mul_f32 v[10:11], v[10:11], s[38:39] op_sel_hi:[1,0]
	v_and_b32_e32 v162, 56, v28
	v_mad_i64_i32 v[14:15], s[6:7], v14, s63, v[44:45]
	v_cvt_pk_bf16_f32 v130, v10, v11
	v_pk_mul_f32 v[10:11], v[16:17], s[38:39] op_sel_hi:[1,0]
	v_lshl_add_u64 v[14:15], v[14:15], 0, s[26:27]
	v_lshlrev_b32_e32 v16, 1, v162
	v_mov_b32_e32 v17, v3
	v_lshl_add_u64 v[18:19], v[14:15], 0, v[16:17]
	s_barrier
; #define LAS __attribute__((address_space(3)))
; #define LDS_WAIT() asm volatile("s_waitcnt lgkmcnt(0)" ::: "memory")
; __device__ __forceinline__ void cvt8(const u32x4 r, float (&f)[8]) { f[0] = bflo(r.x); f[1] = bfhi(r.x); f[2] = bflo(r.y); f[3] = bfhi(r.y); f[4] = bflo(r.z); f[5] = bfhi(r.z); f[6] = bflo(r.w); f[7] = bfhi(r.w); }
; __device__ __forceinline__ bf16x8 pack8(const float (&f)[8]) { u32x4 w; w.x = pk2(f[0], f[1]); w.y = pk2(f[2], f[3]); w.z = pk2(f[4], f[5]); w.w = pk2(f[6], f[7]); return __builtin_bit_cast(bf16x8, w); }
; __device__ __forceinline__ void attn_unit(Ctx& C, int l, int uidx) {
;     ...
;     { const float sk = INP(I_SINK)[l * 8 + head] * LOG2E; m_[0] = sk; m_[1] = sk; l_[0] = 1.f; l_[1] = 1.f; }
; #pragma unroll
;     for (int a = 0; a < 2; ++a)
; #pragma unroll
;         for (int q = 0; q < 2; ++q)
; #pragma unroll
;             for (int i = 0; i < 16; ++i) O[a][q][i] = 0.f;
;     ...
;     __syncthreads();
;     u32x4 kraw[2], kpar[2], vraw[2];
;     kpar[0] = (u32x4){0u, 0u, 0u, 0u}; kpar[1] = kpar[0];
;     int tt = isctx ? 3 : (nb == 0 ? 1 : 0);
;     AT_PREFETCH(tt);
;     while (tt < 5) {
;         int ntt = tt + 1; if (ntt < 3 && !AT_VALID(ntt)) ntt = 3;
;         const bool band = tt < 3; const int kb = nb - 1 + tt;
;         LDS_WAIT(); __builtin_amdgcn_s_barrier(); asm volatile("" ::: "memory");
; #pragma unroll
;         for (int r = 0; r < 2; ++r) {
;             const int idx = C.tid + 512 * r, key = idx >> 3, cd = idx & 7;
;             u32x4 raw = kraw[r];
;             if (band) {
;                 float x[8], y[8]; cvt8(raw, x); cvt8(kpar[r], y);
;                 const int tk = 128 * kb + key, pos = (cd & 4) ? (tk & 63) : (tk >> 6), i0 = 8 * (cd & 1); const bool isb = (cd >> 1) & 1;
; #pragma unroll
;                 for (int j = 0; j < 8; ++j) { const f32x2 cs = ROPE[pos * 16 + i0 + j]; x[j] = isb ? (x[j] * cs.x + y[j] * cs.y) : (x[j] * cs.x - y[j] * cs.y); }
;                 raw = __builtin_bit_cast(u32x4, pack8(x));
;             }
;             *(LAS u32x4*)(C.lds + key * KS + cd * 16) = raw;
;             const u32x4 vr = vraw[r];
;             LAS bf16* vt = (LAS bf16*)(C.lds + VT_OFF + (8 * cd) * VS + key * 2);
	global_load_dwordx4 v[144:147], v[18:19], off offset:2048
	global_load_dwordx4 v[148:151], v[18:19], off offset:2304
	v_add_u32_e32 v18, 0x200, v172
	v_ashrrev_i32_e32 v174, 3, v18
	v_bitop3_b32 v164, v28, 16, 56 bitop3:0x6c
	v_add_u32_e32 v18, v174, v25
	v_lshlrev_b32_e32 v20, 1, v164
	v_mov_b32_e32 v21, v3
	v_mad_i64_i32 v[18:19], s[6:7], v18, s63, v[44:45]
	v_lshl_add_u64 v[14:15], v[14:15], 0, v[20:21]
	v_lshl_add_u64 v[18:19], v[18:19], 0, s[26:27]
	v_lshl_add_u64 v[16:17], v[18:19], 0, v[16:17]
	global_load_dwordx4 v[132:135], v[14:15], off offset:2048
	global_load_dwordx4 v[152:155], v[16:17], off offset:2048
	v_lshl_add_u64 v[14:15], v[18:19], 0, v[20:21]
	global_load_dwordx4 v[136:139], v[14:15], off offset:2048
	global_load_dwordx4 v[156:159], v[16:17], off offset:2304
	v_lshlrev_b32_e32 v14, 16, v39
	v_and_b32_e32 v15, 0xffff0000, v39
	v_mov_b32_e32 v16, v26
	s_waitcnt vmcnt(7)
	v_mov_b32_e32 v17, v4
	v_lshlrev_b32_e32 v12, 16, v43
	v_and_b32_e32 v13, 0xffff0000, v43
	v_pk_mul_f32 v[18:19], v[16:17], v[14:15]
	v_mov_b32_e32 v4, v27
	v_pk_fma_f32 v[18:19], v[4:5], v[12:13], v[18:19]
	v_pk_mul_f32 v[4:5], v[4:5], v[14:15]
	v_cvt_pk_bf16_f32 v140, v6, v7
	v_pk_fma_f32 v[4:5], v[16:17], v[12:13], v[4:5] neg_lo:[0,0,1] neg_hi:[0,0,1]
	v_and_b32_e32 v6, 4, v172
	v_pk_mul_f32 v[4:5], v[4:5], s[38:39] op_sel_hi:[1,0]
	v_cmp_eq_u32_e64 s[6:7], 0, v6
	v_cvt_pk_bf16_f32 v131, v4, v5
	v_pk_mul_f32 v[4:5], v[18:19], s[38:39] op_sel_hi:[1,0]
	v_and_b32_e32 v6, 2, v172
	v_cvt_pk_bf16_f32 v143, v4, v5
	v_mul_u32_u24_e32 v4, 0x108, v48
	v_add_u32_e32 v4, v4, v49
	v_add_u32_e32 v178, s72, v4
	v_or_b32_e32 v4, s54, v48
	v_sub_u32_e32 v4, v4, v175
	v_and_b32_e32 v5, 7, v172
	v_add_u32_e32 v179, 4, v4
	v_mul_u32_u24_e32 v4, 0x90, v48
	s_lshl_b32 s34, s9, 1
	s_sub_i32 s60, 32, s8
	v_cmp_eq_u32_e64 s[8:9], 0, v6
	v_mul_lo_u32 v6, v173, s70
	v_lshlrev_b32_e32 v19, 4, v5
	v_mul_u32_u24_e32 v20, 0x840, v5
	v_mul_lo_u32 v5, v174, s70
	v_add3_u32 v180, v4, v2, 0
	v_sub_u32_e32 v2, v175, v48
	v_readfirstlane_b32 s18, v23
	s_addk_i32 s19, 0x3e80
	s_or_b32 s35, s34, 1
	v_add_u32_e32 v18, 0, v6
	v_lshlrev_b32_e32 v21, 1, v173
	v_lshlrev_b32_e32 v23, 1, v174
	v_subrev_u32_e32 v2, s54, v2
	v_mov_b32_e32 v16, v3
	v_mov_b32_e32 v17, v3
	v_cvt_pk_bf16_f32 v117, v64, v65
	v_cvt_pk_bf16_f32 v141, v8, v9
	v_cvt_pk_bf16_f32 v142, v10, v11
	v_readfirstlane_b32 s61, v24
	v_and_b32_e32 v177, 8, v28
	s_add_u32 s48, s10, s26
	s_waitcnt vmcnt(6)
	v_mul_f32_e32 v187, 0x3fb8aa3b, v22
	v_add_u32_e32 v22, 0, v5
	v_subrev_u32_e32 v181, 31, v2
	v_mov_b32_e32 v2, v3
	v_mov_b32_e32 v4, v3
	v_mov_b32_e32 v5, v3
	v_mov_b32_e32 v6, v3
	v_mov_b32_e32 v7, v3
	v_mov_b32_e32 v8, v3
	v_mov_b32_e32 v9, v3
	v_mov_b32_e32 v10, v3
	v_mov_b32_e32 v11, v3
	v_mov_b32_e32 v12, v3
	v_mov_b32_e32 v13, v3
	v_mov_b32_e32 v14, v3
	v_mov_b32_e32 v15, v3
	v_add_u32_e32 v182, v18, v19
	v_add_u32_e32 v183, v20, v21
	v_add_u32_e32 v184, v22, v19
	v_add_u32_e32 v185, v20, v23
	v_mov_b64_e32 v[32:33], v[16:17]
	v_mov_b64_e32 v[64:65], v[16:17]
	v_mov_b64_e32 v[48:49], v[16:17]
	v_mov_b64_e32 v[80:81], v[16:17]
	v_and_b32_e32 v172, 63, v174
	s_addc_u32 s49, s11, 0
	v_mov_b32_e32 v190, v187
	v_mov_b64_e32 v[30:31], v[14:15]
	v_mov_b64_e32 v[28:29], v[12:13]
	v_mov_b64_e32 v[26:27], v[10:11]
	v_mov_b64_e32 v[24:25], v[8:9]
	v_mov_b64_e32 v[22:23], v[6:7]
	v_mov_b64_e32 v[20:21], v[4:5]
	v_mov_b64_e32 v[18:19], v[2:3]
	v_mov_b64_e32 v[62:63], v[14:15]
	v_mov_b64_e32 v[60:61], v[12:13]
	v_mov_b64_e32 v[58:59], v[10:11]
	v_mov_b64_e32 v[56:57], v[8:9]
	v_mov_b64_e32 v[54:55], v[6:7]
	v_mov_b64_e32 v[52:53], v[4:5]
	v_mov_b64_e32 v[50:51], v[2:3]
	v_mov_b64_e32 v[46:47], v[14:15]
	v_mov_b64_e32 v[44:45], v[12:13]
	v_mov_b64_e32 v[42:43], v[10:11]
	v_mov_b64_e32 v[40:41], v[8:9]
	v_mov_b64_e32 v[38:39], v[6:7]
	v_mov_b64_e32 v[36:37], v[4:5]
	v_mov_b64_e32 v[34:35], v[2:3]
	v_mov_b64_e32 v[78:79], v[14:15]
	v_mov_b64_e32 v[76:77], v[12:13]
	v_mov_b64_e32 v[74:75], v[10:11]
	v_mov_b64_e32 v[72:73], v[8:9]
	v_mov_b64_e32 v[70:71], v[6:7]
	v_mov_b64_e32 v[68:69], v[4:5]
	v_mov_b64_e32 v[66:67], v[2:3]

; #define LAS __attribute__((address_space(3)))
; #define LDS_WAIT() asm volatile("s_waitcnt lgkmcnt(0)" ::: "memory")
; __device__ __forceinline__ void cvt8(const u32x4 r, float (&f)[8]) { f[0] = bflo(r.x); f[1] = bfhi(r.x); f[2] = bflo(r.y); f[3] = bfhi(r.y); f[4] = bflo(r.z); f[5] = bfhi(r.z); f[6] = bflo(r.w); f[7] = bfhi(r.w); }
; __device__ __forceinline__ bf16x8 pack8(const float (&f)[8]) { u32x4 w; w.x = pk2(f[0], f[1]); w.y = pk2(f[2], f[3]); w.z = pk2(f[4], f[5]); w.w = pk2(f[6], f[7]); return __builtin_bit_cast(bf16x8, w); }
; __device__ __forceinline__ void attn_unit(Ctx& C, int l, int uidx) {
;     ...
;         LDS_WAIT(); __builtin_amdgcn_s_barrier(); asm volatile("" ::: "memory");
; #pragma unroll
;         for (int r = 0; r < 2; ++r) {
;             const int idx = C.tid + 512 * r, key = idx >> 3, cd = idx & 7;
;             u32x4 raw = kraw[r];
;             if (band) {
;                 float x[8], y[8]; cvt8(raw, x); cvt8(kpar[r], y);
;                 const int tk = 128 * kb + key, pos = (cd & 4) ? (tk & 63) : (tk >> 6), i0 = 8 * (cd & 1); const bool isb = (cd >> 1) & 1;
; #pragma unroll
;                 for (int j = 0; j < 8; ++j) { const f32x2 cs = ROPE[pos * 16 + i0 + j]; x[j] = isb ? (x[j] * cs.x + y[j] * cs.y) : (x[j] * cs.x - y[j] * cs.y); }
;                 raw = __builtin_bit_cast(u32x4, pack8(x));
;             }
;             *(LAS u32x4*)(C.lds + key * KS + cd * 16) = raw;
;             const u32x4 vr = vraw[r];
;             LAS bf16* vt = (LAS bf16*)(C.lds + VT_OFF + (8 * cd) * VS + key * 2);
;             vt[0] = (bf16)(vr.x & 0xffff); vt[VS / 2] = (bf16)(vr.x >> 16); vt[2 * (VS / 2)] = (bf16)(vr.y & 0xffff); vt[3 * (VS / 2)] = (bf16)(vr.y >> 16);
;             vt[4 * (VS / 2)] = (bf16)(vr.z & 0xffff); vt[5 * (VS / 2)] = (bf16)(vr.z >> 16); vt[6 * (VS / 2)] = (bf16)(vr.w & 0xffff); vt[7 * (VS / 2)] = (bf16)(vr.w >> 16);
;         }
.LBB0_1739:
	ds_write_b128 v182, v[4:7]
	s_waitcnt vmcnt(2)
	ds_write_b16 v183, v148 offset:18432
	ds_write_b16_d16_hi v183, v148 offset:18696
	ds_write_b16 v183, v149 offset:18960
	ds_write_b16_d16_hi v183, v149 offset:19224
	ds_write_b16 v183, v150 offset:19488
	ds_write_b16_d16_hi v183, v150 offset:19752
	ds_write_b16 v183, v151 offset:20016
	ds_write_b16_d16_hi v183, v151 offset:20280
	s_waitcnt vmcnt(1)
	v_mov_b64_e32 v[4:5], v[152:153]
	s_andn2_b64 vcc, exec, s[10:11]
	v_mov_b64_e32 v[6:7], v[154:155]
	s_cbranch_vccnz .LBB0_1741
	v_add_u32_e32 v2, s26, v174
	v_ashrrev_i32_e32 v2, 6, v2
	v_cndmask_b32_e64 v2, v172, v2, s[6:7]
	v_lshl_or_b32 v4, v2, 4, v177
	v_ashrrev_i32_e32 v5, 31, v4
	v_lshl_add_u64 v[16:17], v[4:5], 3, s[52:53]
	global_load_dwordx4 v[4:7], v[16:17], off
	global_load_dwordx4 v[8:11], v[16:17], off offset:16
	global_load_dwordx4 v[12:15], v[16:17], off offset:32
	global_load_dwordx4 v[82:85], v[16:17], off offset:48
	s_waitcnt vmcnt(5)
	v_lshlrev_b32_e32 v91, 16, v136
	v_and_b32_e32 v92, 0xffff0000, v136
	v_lshlrev_b32_e32 v93, 16, v137
	v_and_b32_e32 v94, 0xffff0000, v137
	v_lshlrev_b32_e32 v95, 16, v138
	v_and_b32_e32 v96, 0xffff0000, v138
	v_lshlrev_b32_e32 v97, 16, v139
	v_and_b32_e32 v98, 0xffff0000, v139
	v_lshlrev_b32_e32 v2, 16, v152
	v_and_b32_e32 v16, 0xffff0000, v152
	v_lshlrev_b32_e32 v17, 16, v153
	v_and_b32_e32 v86, 0xffff0000, v153
	v_lshlrev_b32_e32 v87, 16, v154
	v_and_b32_e32 v88, 0xffff0000, v154
	v_lshlrev_b32_e32 v89, 16, v155
	v_and_b32_e32 v90, 0xffff0000, v155
	s_waitcnt vmcnt(3)
	v_mul_f32_e32 v5, v5, v91
	v_mul_f32_e32 v7, v7, v92
	s_waitcnt vmcnt(2)
	v_mul_f32_e32 v9, v9, v93
	v_mul_f32_e32 v11, v11, v94
	s_waitcnt vmcnt(1)
	v_mul_f32_e32 v13, v13, v95
	v_mul_f32_e32 v15, v15, v96
	s_waitcnt vmcnt(0)
	v_mul_f32_e32 v83, v83, v97
	v_mul_f32_e32 v85, v85, v98
	v_cndmask_b32_e64 v5, v5, -v5, s[8:9]
	v_cndmask_b32_e64 v7, v7, -v7, s[8:9]
	v_cndmask_b32_e64 v9, v9, -v9, s[8:9]
	v_cndmask_b32_e64 v11, v11, -v11, s[8:9]
	v_cndmask_b32_e64 v13, v13, -v13, s[8:9]
	v_cndmask_b32_e64 v15, v15, -v15, s[8:9]
	v_cndmask_b32_e64 v83, v83, -v83, s[8:9]
	v_cndmask_b32_e64 v85, v85, -v85, s[8:9]
	v_fmac_f32_e32 v5, v4, v2
	v_fmac_f32_e32 v7, v6, v16
	v_fmac_f32_e32 v9, v8, v17
	v_fmac_f32_e32 v11, v10, v86
	v_fmac_f32_e32 v13, v12, v87
	v_fmac_f32_e32 v15, v14, v88
	v_fmac_f32_e32 v83, v82, v89
	v_fmac_f32_e32 v85, v84, v90
	v_cvt_pk_bf16_f32 v4, v5, v7
	v_cvt_pk_bf16_f32 v5, v9, v11
	v_cvt_pk_bf16_f32 v6, v13, v15
	v_cvt_pk_bf16_f32 v7, v83, v85
.LBB0_1741:
	s_cmp_gt_i32 s61, 1
	s_cselect_b64 s[10:11], -1, 0
	s_cmp_lt_u32 s61, s60
	s_cselect_b64 s[54:55], -1, 0
	s_or_b64 s[10:11], s[10:11], s[54:55]
	s_add_i32 s26, s61, 1
	s_and_b64 s[10:11], s[10:11], exec
	s_cselect_b32 s26, s26, 3
	s_cmp_gt_i32 s26, 4
	s_cselect_b64 s[54:55], -1, 0
	s_and_b64 vcc, exec, s[54:55]
	ds_write_b128 v184, v[4:7]
	s_waitcnt vmcnt(0)
	ds_write_b16 v185, v156 offset:18432
	ds_write_b16_d16_hi v185, v156 offset:18696
	ds_write_b16 v185, v157 offset:18960
	ds_write_b16_d16_hi v185, v157 offset:19224
	ds_write_b16 v185, v158 offset:19488
	ds_write_b16_d16_hi v185, v158 offset:19752
	ds_write_b16 v185, v159 offset:20016
	ds_write_b16_d16_hi v185, v159 offset:20280
	s_cbranch_vccnz .LBB0_1751
	s_cmp_lt_i32 s26, 3
	s_cselect_b64 s[56:57], -1, 0
	s_cmp_gt_i32 s26, 2
	s_mov_b64 s[10:11], -1
	s_cbranch_scc0 .LBB0_1744
	s_lshl_b32 s10, s26, 7
	s_add_i32 s74, s19, s10
	s_mov_b64 s[10:11], 0

; #define LAS __attribute__((address_space(3)))
; __device__ __forceinline__ float xor32_sum(float x) { const auto r = __builtin_amdgcn_permlane32_swap(__float_as_uint(x), __float_as_uint(x), false, false); return __uint_as_float(r[0]) + __uint_as_float(r[1]); }
; __device__ __forceinline__ float xor32_max(float x) { const auto r = __builtin_amdgcn_permlane32_swap(__float_as_uint(x), __float_as_uint(x), false, false); return fmaxf(__uint_as_float(r[0]), __uint_as_float(r[1])); }
; __device__ __forceinline__ void attn_unit(Ctx& C, int l, int uidx) {
;     ...
;                 const int tq = 128 * nb + 64 * th + 32 * qb + r32;
;                 float mx = -INFINITY;
; #pragma unroll
;                 for (int i = 0; i < 16; ++i) { float x = S[i];
;                     if (tt == 0 || tt == 2) { const int kpos = 128 * kb + 32 * sub + (i & 3) + 8 * (i >> 2) + 4 * h; const int dq = tq - kpos; if (dq > 128 || dq < -128) x = -INFINITY; }
;                     S[i] = x; mx = fmaxf(mx, x); }
;                 mx = xor32_max(mx);
;                 const float mnew = fmaxf(m_[qb], mx), alpha = __builtin_amdgcn_exp2f(m_[qb] - mnew);
;                 float rs = 0.f; float p[16];
; #pragma unroll
;                 for (int i = 0; i < 16; ++i) { p[i] = __builtin_amdgcn_exp2f(S[i] - mnew); rs += p[i]; }
;                 rs = xor32_sum(rs);
;                 l_[qb] = l_[qb] * alpha + rs; m_[qb] = mnew;
; #pragma unroll
;                 for (int i = 0; i < 16; ++i) { O[0][qb][i] *= alpha; O[1][qb][i] *= alpha; }
; #pragma unroll
;                 for (int s2 = 0; s2 < 2; ++s2) { float t8[8];
; #pragma unroll
;                     for (int j = 0; j < 8; ++j) t8[j] = p[8 * s2 + j];
;                     Pf[qb][s2] = pack8(t8); }
;             }
; #pragma unroll
;             for (int db = 0; db < 2; ++db)
; #pragma unroll
;                 for (int s2 = 0; s2 < 2; ++s2) {
;                     const LAS unsigned char* vp = C.lds + VT_OFF + (32 * db + r32) * VS + (32 * sub + 16 * s2 + 4 * h) * 2;
;                     const u32x2 v0 = *(const LAS u32x2*)vp, v1 = *(const LAS u32x2*)(vp + 16);
;                     const u32x4 vv = {v0.x, v0.y, v1.x, v1.y}; const bf16x8 Vf = __builtin_bit_cast(bf16x8, vv);
;                     O[db][0] = MFMA32(Vf, Pf[0][s2], O[db][0]); O[db][1] = MFMA32(Vf, Pf[1][s2], O[db][1]);
;                 }
.Lattn_l1_nomask2:
.LBB0_1915:
	v_max3_f32 v2, v82, s76, v83
	v_max3_f32 v2, v2, v84, v85
	v_max3_f32 v2, v2, v86, v87
	v_max3_f32 v2, v2, v88, v89
	v_max3_f32 v4, v2, v90, v91
	v_sub_f32_e32 v2, v190, v191
	v_exp_f32_e32 v2, v2
	v_max3_f32 v4, v4, v92, v93
	v_max3_f32 v7, v4, v94, v95
	v_add_f32_e32 v100, v8, v9
	v_fmac_f32_e32 v100, v189, v2
	v_pk_mul_f32 v[80:81], v[80:81], v[2:3] op_sel_hi:[1,0]
	v_pk_mul_f32 v[78:79], v[78:79], v[2:3] op_sel_hi:[1,0]
	v_pk_mul_f32 v[76:77], v[76:77], v[2:3] op_sel_hi:[1,0]
	v_pk_mul_f32 v[74:75], v[74:75], v[2:3] op_sel_hi:[1,0]
	v_pk_mul_f32 v[72:73], v[72:73], v[2:3] op_sel_hi:[1,0]
	v_pk_mul_f32 v[70:71], v[70:71], v[2:3] op_sel_hi:[1,0]
	v_pk_mul_f32 v[68:69], v[68:69], v[2:3] op_sel_hi:[1,0]
	v_pk_mul_f32 v[66:67], v[66:67], v[2:3] op_sel_hi:[1,0]
	v_pk_mul_f32 v[64:65], v[64:65], v[2:3] op_sel_hi:[1,0]
	v_pk_mul_f32 v[62:63], v[62:63], v[2:3] op_sel_hi:[1,0]
	v_pk_mul_f32 v[60:61], v[60:61], v[2:3] op_sel_hi:[1,0]
	v_pk_mul_f32 v[58:59], v[58:59], v[2:3] op_sel_hi:[1,0]
	v_pk_mul_f32 v[56:57], v[56:57], v[2:3] op_sel_hi:[1,0]
	v_pk_mul_f32 v[54:55], v[54:55], v[2:3] op_sel_hi:[1,0]
	v_pk_mul_f32 v[52:53], v[52:53], v[2:3] op_sel_hi:[1,0]
	v_pk_mul_f32 v[50:51], v[50:51], v[2:3] op_sel_hi:[1,0]
	v_max3_f32 v2, v7, v96, v97
	v_mov_b32_e32 v7, v2
	s_nop 1
	v_permlane32_swap_b32_e32 v2, v7
	v_cvt_pk_bf16_f32 v6, v14, v15
	v_max3_f32 v14, v187, v2, v7
	v_sub_f32_e32 v2, v82, v14
	v_sub_f32_e32 v82, v85, v14
	v_cvt_pk_bf16_f32 v5, v98, v99
	v_exp_f32_e32 v99, v82
	v_sub_f32_e32 v82, v86, v14
	v_exp_f32_e32 v101, v82
	v_sub_f32_e32 v82, v87, v14
	v_exp_f32_e32 v102, v82
	v_sub_f32_e32 v82, v88, v14
	v_exp_f32_e32 v15, v2
	v_sub_f32_e32 v2, v83, v14
	v_exp_f32_e32 v103, v82
	v_sub_f32_e32 v82, v89, v14
	v_exp_f32_e32 v98, v2
	v_sub_f32_e32 v2, v187, v14
	v_exp_f32_e32 v187, v82
	v_sub_f32_e32 v82, v90, v14
	v_exp_f32_e32 v189, v82
	v_sub_f32_e32 v82, v91, v14
	v_exp_f32_e32 v190, v82
	v_sub_f32_e32 v82, v92, v14
	v_cvt_pk_bf16_f32 v7, v12, v13
	v_sub_f32_e32 v13, v84, v14
	v_exp_f32_e32 v193, v82
	ds_read2_b64 v[82:85], v16 offset1:2
	v_exp_f32_e32 v13, v13
	v_exp_f32_e32 v2, v2
	v_sub_f32_e32 v86, v93, v14
	v_cvt_pk_bf16_f32 v8, v194, v195
	v_cvt_pk_bf16_f32 v9, v196, v197
	v_cvt_pk_bf16_f32 v10, v198, v199
	v_cvt_pk_bf16_f32 v11, v200, v201
	v_exp_f32_e32 v194, v86
	v_pk_mul_f32 v[48:49], v[48:49], v[2:3] op_sel_hi:[1,0]
	v_pk_mul_f32 v[46:47], v[46:47], v[2:3] op_sel_hi:[1,0]
	v_pk_mul_f32 v[44:45], v[44:45], v[2:3] op_sel_hi:[1,0]
	v_pk_mul_f32 v[42:43], v[42:43], v[2:3] op_sel_hi:[1,0]
	v_pk_mul_f32 v[40:41], v[40:41], v[2:3] op_sel_hi:[1,0]
	v_pk_mul_f32 v[38:39], v[38:39], v[2:3] op_sel_hi:[1,0]
	v_pk_mul_f32 v[36:37], v[36:37], v[2:3] op_sel_hi:[1,0]
	v_pk_mul_f32 v[34:35], v[34:35], v[2:3] op_sel_hi:[1,0]
	v_cvt_pk_bf16_f32 v86, v15, v98
	v_cvt_pk_bf16_f32 v87, v13, v99
	v_cvt_pk_bf16_f32 v88, v101, v102
	v_cvt_pk_bf16_f32 v89, v103, v187
	v_add_f32_e32 v12, 0, v15
	s_waitcnt lgkmcnt(0)
	v_mfma_f32_32x32x16_bf16 v[66:81], v[82:85], v[8:11], v[66:81]
	v_add_f32_e32 v12, v98, v12
	v_add_u32_e32 v197, 0x2000, v16
	v_sub_f32_e32 v15, v94, v14
	v_add_f32_e32 v12, v13, v12
	ds_read2_b64 v[90:93], v16 offset0:4 offset1:6
	v_add_f32_e32 v12, v99, v12
	v_pk_mul_f32 v[32:33], v[32:33], v[2:3] op_sel_hi:[1,0]
	v_mfma_f32_32x32x16_bf16 v[34:49], v[82:85], v[86:89], v[34:49]
	v_sub_f32_e32 v82, v95, v14
	v_exp_f32_e32 v98, v82
	v_sub_f32_e32 v82, v96, v14
	v_exp_f32_e32 v195, v82
	v_sub_f32_e32 v82, v97, v14
	ds_read2_b64 v[94:97], v197 offset0:32 offset1:34
	v_pk_mul_f32 v[30:31], v[30:31], v[2:3] op_sel_hi:[1,0]
	s_waitcnt lgkmcnt(0)
	v_mfma_f32_32x32x16_bf16 v[50:65], v[94:97], v[8:11], v[50:65]
	v_mul_f32_e64 v28, v28, v2
	v_mul_f32_e64 v29, v29, v2
	v_mul_f32_e64 v26, v26, v2
	v_mul_f32_e64 v27, v27, v2
	v_mul_f32_e64 v24, v24, v2
	v_mul_f32_e64 v25, v25, v2
	v_pk_mul_f32 v[22:23], v[22:23], v[2:3] op_sel_hi:[1,0]
	v_pk_mul_f32 v[20:21], v[20:21], v[2:3] op_sel_hi:[1,0]
	v_pk_mul_f32 v[18:19], v[18:19], v[2:3] op_sel_hi:[1,0]
	ds_read2_b64 v[8:11], v197 offset0:36 offset1:38
	v_add_f32_e32 v12, v101, v12
	v_mfma_f32_32x32x16_bf16 v[18:33], v[94:97], v[86:89], v[18:33]
	v_add_f32_e32 v12, v102, v12
	v_add_f32_e32 v12, v103, v12
	v_exp_f32_e32 v15, v15
	v_exp_f32_e32 v196, v82
	v_add_f32_e32 v12, v187, v12
	v_add_f32_e32 v12, v189, v12
	v_add_f32_e32 v12, v190, v12
	v_add_f32_e32 v12, v193, v12
	v_cvt_pk_bf16_f32 v4, v202, v203
	v_cvt_pk_bf16_f32 v82, v189, v190
	v_cvt_pk_bf16_f32 v83, v193, v194
	v_cvt_pk_bf16_f32 v84, v15, v98
	v_cvt_pk_bf16_f32 v85, v195, v196
	v_add_f32_e32 v12, v194, v12
	v_mfma_f32_32x32x16_bf16 v[66:81], v[90:93], v[4:7], v[66:81]
	v_add_f32_e32 v12, v15, v12
	v_add_f32_e32 v12, v98, v12
	s_add_i32 s87, s87, 1
	v_add_u32_e32 v16, 64, v16
	s_cmp_ge_u32 s87, s74
	v_add_u32_e32 v17, 0x1200, v17
	v_mfma_f32_32x32x16_bf16 v[34:49], v[90:93], v[82:85], v[34:49]
	s_waitcnt lgkmcnt(0)
	v_mfma_f32_32x32x16_bf16 v[50:65], v[8:11], v[4:7], v[50:65]
	v_add_f32_e32 v4, v195, v12
	v_add_f32_e32 v4, v196, v4
	v_mov_b32_e32 v5, v4
	s_nop 1
	v_permlane32_swap_b32_e32 v4, v5
	v_add_f32_e32 v4, v4, v5
	v_fmac_f32_e32 v4, v186, v2
	v_mfma_f32_32x32x16_bf16 v[18:33], v[8:11], v[82:85], v[18:33]
	s_cbranch_scc1 .LBB0_1948
	v_mov_b32_e32 v193, v188
	v_mov_b32_e32 v2, v192
	v_mov_b32_e32 v187, v14
	v_mov_b32_e32 v190, v191
	v_mov_b32_e32 v186, v4
	v_mov_b32_e32 v189, v100
	s_branch .LBB0_1753
